# latent attention QK^T: K fragments read three pairs ahead into unused VGPRs v226-249 (was one pair ahead into time-shared registers); on top of the barrier change
# baseline (speedup 1.0000x reference)
; #define MLA_PIN(x) asm volatile("" : "+v"(x))
; template <int THRL, bool LATE> __device__ __forceinline__ void unit_stag(int b, int h, int qb, const unsigned short* Q, const unsigned short* KV, const unsigned short* KPE, unsigned short* O, char* shm, const int wave_) {
;     ...
;     { const float rm_ = rowmax(pA0, pA1); mhat = rm_;
; #pragma unroll
;       for (int r = 0; r < 16; ++r) { pA0[r] -= rm_; pA1[r] -= rm_; negm[r] = -mhat; }
;       MLA_PIN(negm); }
;     int t = 0;
;     MLA_STEPS(pB0, pB1, pA0, pA1, t, -1, 3, true, true, false); ++t;
.LBB0_1103:
	s_or_b64 exec, exec, s[0:1]
	s_and_b32 s0, s10, 0x3fffffc0
	s_lshl_b32 s0, s0, 2
	s_add_i32 s74, s0, 0
	s_add_i32 s74, s74, 0x11000
	s_cmp_lg_u32 0, -1
	s_cselect_b32 s0, 0, 0
	s_add_i32 s0, s0, s42
	v_sub_f32_e32 v96, v2, v154
	v_sub_f32_e32 v97, v3, v154
	v_lshl_add_u64 v[2:3], v[156:157], 0, s[18:19]
	s_add_i32 s0, s0, 0xd000
	s_mov_b32 s1, m0
	s_mov_b32 m0, s0
	s_nop 0
	global_load_lds_dwordx4 v[2:3], off
	s_mov_b32 m0, s1
	v_sub_f32_e32 v0, v18, v154
	v_sub_f32_e32 v19, v19, v154
	v_sub_f32_e32 v20, v20, v154
	v_sub_f32_e32 v98, v4, v154
	v_sub_f32_e32 v4, v21, v154
	v_sub_f32_e32 v99, v5, v154
	v_pk_add_f32 v[22:23], v[22:23], v[154:155] op_sel_hi:[1,0] neg_lo:[0,1] neg_hi:[0,1]
	v_pk_add_f32 v[6:7], v[6:7], v[154:155] op_sel_hi:[1,0] neg_lo:[0,1] neg_hi:[0,1]
	v_pk_add_f32 v[24:25], v[24:25], v[154:155] op_sel_hi:[1,0] neg_lo:[0,1] neg_hi:[0,1]
	v_pk_add_f32 v[8:9], v[8:9], v[154:155] op_sel_hi:[1,0] neg_lo:[0,1] neg_hi:[0,1]
	v_pk_add_f32 v[26:27], v[26:27], v[154:155] op_sel_hi:[1,0] neg_lo:[0,1] neg_hi:[0,1]
	v_pk_add_f32 v[10:11], v[10:11], v[154:155] op_sel_hi:[1,0] neg_lo:[0,1] neg_hi:[0,1]
	v_pk_add_f32 v[28:29], v[28:29], v[154:155] op_sel_hi:[1,0] neg_lo:[0,1] neg_hi:[0,1]
	v_pk_add_f32 v[12:13], v[12:13], v[154:155] op_sel_hi:[1,0] neg_lo:[0,1] neg_hi:[0,1]
	v_pk_add_f32 v[30:31], v[30:31], v[154:155] op_sel_hi:[1,0] neg_lo:[0,1] neg_hi:[0,1]
	v_pk_add_f32 v[14:15], v[14:15], v[154:155] op_sel_hi:[1,0] neg_lo:[0,1] neg_hi:[0,1]
	v_pk_add_f32 v[32:33], v[32:33], v[154:155] op_sel_hi:[1,0] neg_lo:[0,1] neg_hi:[0,1]
	v_pk_add_f32 v[16:17], v[16:17], v[154:155] op_sel_hi:[1,0] neg_lo:[0,1] neg_hi:[0,1]
	s_setprio 1
	ds_read_b128 v[226:229], v173 offset:12288
	ds_read_b128 v[230:233], v173 offset:12800
	ds_read_b128 v[234:237], v173 offset:14336
	ds_read_b128 v[238:241], v173 offset:14848
	ds_read_b128 v[242:245], v173 offset:16384
	ds_read_b128 v[246:249], v173 offset:16896
	v_exp_f32_e32 v21, v4
	v_exp_f32_e32 v18, v0
	v_exp_f32_e32 v19, v19
	v_exp_f32_e32 v20, v20
	s_nop 0
	v_exp_f32_e32 v22, v22
	v_exp_f32_e32 v23, v23
	v_exp_f32_e32 v24, v24
	v_exp_f32_e32 v25, v25
	s_waitcnt lgkmcnt(5)
	v_mfma_f32_32x32x16_bf16 v[66:81], v[226:229], v[150:153], v[34:49]
	v_exp_f32_e32 v26, v26
	v_exp_f32_e32 v27, v27
	v_exp_f32_e32 v28, v28
	v_exp_f32_e32 v29, v29
	v_mov_b64_e32 v[64:65], v[48:49]
	v_mov_b64_e32 v[62:63], v[46:47]
	v_mov_b64_e32 v[60:61], v[44:45]
	v_mov_b64_e32 v[58:59], v[42:43]
	v_mov_b64_e32 v[56:57], v[40:41]
	v_mov_b64_e32 v[54:55], v[38:39]
	v_mov_b64_e32 v[52:53], v[36:37]
	v_mov_b64_e32 v[50:51], v[34:35]
	v_exp_f32_e32 v30, v30
	v_exp_f32_e32 v31, v31
	s_waitcnt lgkmcnt(4)
	v_mfma_f32_32x32x16_bf16 v[50:65], v[230:233], v[150:153], v[50:65]
	ds_read_b128 v[226:229], v173 offset:18432
	ds_read_b128 v[230:233], v173 offset:18944
	v_exp_f32_e32 v32, v32
	v_exp_f32_e32 v33, v33
	s_nop 0
	v_add_f32_e32 v0, 0, v18
	v_add_f32_e32 v0, v19, v0
	v_add_f32_e32 v0, v20, v0
	v_add_f32_e32 v0, v21, v0
	s_waitcnt lgkmcnt(5)
	v_mfma_f32_32x32x16_bf16 v[66:81], v[234:237], v[146:149], v[66:81]
	v_exp_f32_e32 v2, v96
	v_exp_f32_e32 v3, v97
	v_exp_f32_e32 v4, v98
	v_exp_f32_e32 v5, v99
	v_add_f32_e32 v0, v0, v22
	v_add_f32_e32 v0, v23, v0
	v_add_f32_e32 v0, v24, v0
	v_add_f32_e32 v0, v25, v0
	s_waitcnt lgkmcnt(4)
	v_mfma_f32_32x32x16_bf16 v[50:65], v[238:241], v[146:149], v[50:65]
	ds_read_b128 v[234:237], v173 offset:20480
	ds_read_b128 v[238:241], v173 offset:20992
	v_add_f32_e32 v0, v26, v0
	v_add_f32_e32 v0, v27, v0
	v_add_f32_e32 v0, v28, v0
	v_exp_f32_e32 v6, v6
	v_exp_f32_e32 v7, v7
	v_exp_f32_e32 v8, v8
	v_exp_f32_e32 v9, v9
	v_add_f32_e32 v0, v29, v0
	v_cvt_pk_bf16_f32 v114, v18, v19
	v_cvt_pk_bf16_f32 v115, v20, v21
	s_waitcnt lgkmcnt(5)
	v_mfma_f32_32x32x16_bf16 v[66:81], v[242:245], v[142:145], v[66:81]
	v_add_f32_e32 v0, v30, v0
	v_add_f32_e32 v0, v31, v0
	v_add_f32_e32 v0, v32, v0
	v_exp_f32_e32 v10, v10
	v_exp_f32_e32 v11, v11
	v_exp_f32_e32 v12, v12
	v_exp_f32_e32 v13, v13
	v_add_f32_e32 v0, v33, v0
	v_cvt_pk_bf16_f32 v116, v22, v23
	v_cvt_pk_bf16_f32 v117, v24, v25
	s_waitcnt lgkmcnt(4)
	v_mfma_f32_32x32x16_bf16 v[50:65], v[246:249], v[142:145], v[50:65]
	ds_read_b128 v[242:245], v173 offset:22528
	ds_read_b128 v[246:249], v173 offset:23040
	v_exp_f32_e32 v14, v14
	v_exp_f32_e32 v15, v15
	v_exp_f32_e32 v16, v16
	v_exp_f32_e32 v17, v17
	v_cvt_pk_bf16_f32 v118, v26, v27
	v_add_f32_e32 v0, v0, v2
	v_add_f32_e32 v0, v3, v0
	v_add_f32_e32 v0, v4, v0
	v_add_f32_e32 v0, v5, v0
	v_cvt_pk_bf16_f32 v119, v28, v29
	s_waitcnt lgkmcnt(5)
	v_mfma_f32_32x32x16_bf16 v[66:81], v[226:229], v[138:141], v[66:81]
	v_add_f32_e32 v0, v0, v6
	v_add_f32_e32 v0, v7, v0
	v_add_f32_e32 v0, v8, v0
	v_add_f32_e32 v0, v9, v0
	v_cvt_pk_bf16_f32 v120, v30, v31
	v_cvt_pk_bf16_f32 v121, v32, v33
	s_waitcnt lgkmcnt(4)
	v_mfma_f32_32x32x16_bf16 v[50:65], v[230:233], v[138:141], v[50:65]
	v_add_f32_e32 v0, v10, v0
	v_add_f32_e32 v0, v11, v0
	v_add_f32_e32 v0, v12, v0
	v_add_f32_e32 v0, v13, v0
	v_cvt_pk_bf16_f32 v122, v2, v3
	v_cvt_pk_bf16_f32 v123, v4, v5
	s_waitcnt lgkmcnt(3)
	v_mfma_f32_32x32x16_bf16 v[66:81], v[234:237], v[134:137], v[66:81]
	v_add_f32_e32 v0, v14, v0
	v_add_f32_e32 v0, v15, v0
	v_add_f32_e32 v0, v16, v0
	v_add_f32_e32 v0, v17, v0
	v_cvt_pk_bf16_f32 v124, v6, v7
	v_cvt_pk_bf16_f32 v125, v8, v9
	s_waitcnt lgkmcnt(2)
	v_mfma_f32_32x32x16_bf16 v[50:65], v[238:241], v[134:137], v[50:65]
	v_cvt_pk_bf16_f32 v126, v10, v11
	v_cvt_pk_bf16_f32 v127, v12, v13
	s_waitcnt lgkmcnt(1)
	v_mfma_f32_32x32x16_bf16 v[66:81], v[242:245], v[130:133], v[66:81]
	v_cvt_pk_bf16_f32 v128, v14, v15
	v_cvt_pk_bf16_f32 v129, v16, v17
	s_waitcnt lgkmcnt(0)
	v_mfma_f32_32x32x16_bf16 v[50:65], v[246:249], v[130:133], v[50:65]
	v_add_f32_e32 v175, 0, v0
	s_setprio 0
	v_max3_f32 v0, v66, v67, v50
	v_max3_f32 v2, v68, v69, v51
	s_nop 0
	v_max3_f32 v0, v0, v52, v53
	v_max3_f32 v2, v2, v72, v73
	s_nop 0
	v_max3_f32 v0, v0, v70, v71
	v_max3_f32 v2, v2, v56, v57
	s_nop 0
	v_max3_f32 v0, v0, v54, v55
	v_max3_f32 v2, v2, v76, v77
	s_nop 0
	v_max3_f32 v0, v0, v74, v75
	v_max3_f32 v2, v2, v60, v61
	s_nop 0
	v_max3_f32 v0, v0, v58, v59
	v_max3_f32 v2, v2, v80, v81
	s_nop 0
	v_max3_f32 v0, v0, v78, v79
	v_max3_f32 v2, v2, v64, v65
	s_nop 0
	v_max3_f32 v0, v0, v62, v63
	v_max_f32_e32 v2, v2, v2
	v_max_f32_e32 v0, v0, v0
	v_max_f32_e32 v0, v0, v2
	v_mov_b32_e32 v2, v0
	s_nop 1
	v_permlane32_swap_b32_e32 v0, v2
	v_max_f32_e32 v2, v2, v2
	v_max_f32_e32 v0, v0, v0
	v_max_f32_e32 v0, v0, v2
	v_cmp_lt_f32_e32 vcc, s54, v0
	s_cmp_lg_u64 vcc, 0
	s_cselect_b64 s[42:43], -1, 0
	s_cbranch_vccnz .LBB0_1205

.LBB0_1109:
	s_or_b64 exec, exec, s[42:43]
	s_add_i32 s42, s82, 0xffffe000
	s_and_b32 s70, s42, 0x6000
	v_lshl_add_u64 v[166:167], v[156:157], 0, s[0:1]
	s_add_i32 s73, s70, s72
	s_mov_b32 s42, m0
	s_mov_b32 m0, s73
	s_nop 0
	global_load_lds_dwordx4 v[166:167], off
	s_mov_b32 m0, s42
	s_mul_i32 s86, s83, 0x3000
	v_add_u32_e32 v185, s86, v173
	s_setprio 1
	ds_read_b128 v[226:229], v185
	ds_read_b128 v[230:233], v185 offset:512
	ds_read_b128 v[234:237], v185 offset:2048
	ds_read_b128 v[238:241], v185 offset:2560
	ds_read_b128 v[242:245], v185 offset:4096
	ds_read_b128 v[246:249], v185 offset:4608
	v_exp_f32_e32 v66, v66
	v_exp_f32_e32 v67, v67
	v_exp_f32_e32 v68, v68
	v_exp_f32_e32 v69, v69
	s_nop 0
	v_exp_f32_e32 v70, v70
	v_exp_f32_e32 v71, v71
	v_exp_f32_e32 v72, v72
	v_exp_f32_e32 v73, v73
	s_waitcnt lgkmcnt(5)
	v_mfma_f32_32x32x16_bf16 v[98:113], v[226:229], v[150:153], v[34:49]
	v_exp_f32_e32 v74, v74
	v_exp_f32_e32 v75, v75
	v_exp_f32_e32 v76, v76
	v_exp_f32_e32 v77, v77
	s_waitcnt lgkmcnt(4)
	v_mfma_f32_32x32x16_bf16 v[82:97], v[230:233], v[150:153], v[34:49]
	ds_read_b128 v[226:229], v185 offset:6144
	ds_read_b128 v[230:233], v185 offset:6656
	v_exp_f32_e32 v78, v78
	v_exp_f32_e32 v79, v79
	v_exp_f32_e32 v80, v80
	v_exp_f32_e32 v81, v81
	s_nop 0
	v_add_f32_e32 v0, 0, v66
	v_add_f32_e32 v0, v67, v0
	v_add_f32_e32 v0, v68, v0
	v_add_f32_e32 v0, v69, v0
	s_waitcnt lgkmcnt(5)
	v_mfma_f32_32x32x16_bf16 v[98:113], v[234:237], v[146:149], v[98:113]
	v_add_f32_e32 v0, v0, v70
	v_add_f32_e32 v0, v71, v0
	v_add_f32_e32 v0, v72, v0
	v_exp_f32_e32 v50, v50
	v_exp_f32_e32 v51, v51
	v_exp_f32_e32 v52, v52
	v_exp_f32_e32 v53, v53
	v_add_f32_e32 v0, v73, v0
	s_waitcnt lgkmcnt(4)
	v_mfma_f32_32x32x16_bf16 v[82:97], v[238:241], v[146:149], v[82:97]
	ds_read_b128 v[234:237], v185 offset:8192
	ds_read_b128 v[238:241], v185 offset:8704
	v_add_f32_e32 v0, v74, v0
	v_add_f32_e32 v0, v75, v0
	v_add_f32_e32 v0, v76, v0
	v_exp_f32_e32 v54, v54
	v_exp_f32_e32 v55, v55
	v_exp_f32_e32 v56, v56
	v_exp_f32_e32 v57, v57
	v_add_f32_e32 v0, v77, v0
	v_cvt_pk_bf16_f32 v114, v66, v67
	v_cvt_pk_bf16_f32 v115, v68, v69
	s_waitcnt lgkmcnt(5)
	v_mfma_f32_32x32x16_bf16 v[98:113], v[242:245], v[142:145], v[98:113]
	v_add_f32_e32 v0, v78, v0
	v_add_f32_e32 v0, v79, v0
	v_add_f32_e32 v0, v80, v0
	v_exp_f32_e32 v58, v58
	v_exp_f32_e32 v59, v59
	v_exp_f32_e32 v60, v60
	v_exp_f32_e32 v61, v61
	v_add_f32_e32 v0, v81, v0
	v_cvt_pk_bf16_f32 v116, v70, v71
	v_cvt_pk_bf16_f32 v117, v72, v73
	s_waitcnt lgkmcnt(4)
	v_mfma_f32_32x32x16_bf16 v[82:97], v[246:249], v[142:145], v[82:97]
	ds_read_b128 v[242:245], v185 offset:10240
	ds_read_b128 v[246:249], v185 offset:10752
	v_exp_f32_e32 v62, v62
	v_exp_f32_e32 v63, v63
	v_exp_f32_e32 v64, v64
	v_exp_f32_e32 v65, v65
	v_cvt_pk_bf16_f32 v118, v74, v75
	v_add_f32_e32 v0, v0, v50
	v_add_f32_e32 v0, v51, v0
	v_add_f32_e32 v0, v52, v0
	v_add_f32_e32 v0, v53, v0
	v_cvt_pk_bf16_f32 v119, v76, v77
	s_waitcnt lgkmcnt(5)
	v_mfma_f32_32x32x16_bf16 v[98:113], v[226:229], v[138:141], v[98:113]
	v_add_f32_e32 v0, v0, v54
	v_add_f32_e32 v0, v55, v0
	v_add_f32_e32 v0, v56, v0
	v_add_f32_e32 v0, v57, v0
	v_cvt_pk_bf16_f32 v120, v78, v79
	v_cvt_pk_bf16_f32 v121, v80, v81
	s_waitcnt lgkmcnt(4)
	v_mfma_f32_32x32x16_bf16 v[82:97], v[230:233], v[138:141], v[82:97]
	v_add_f32_e32 v0, v58, v0
	v_add_f32_e32 v0, v59, v0
	v_add_f32_e32 v0, v60, v0
	v_add_f32_e32 v0, v61, v0
	v_cvt_pk_bf16_f32 v122, v50, v51
	v_cvt_pk_bf16_f32 v123, v52, v53
	s_waitcnt lgkmcnt(3)
	v_mfma_f32_32x32x16_bf16 v[98:113], v[234:237], v[134:137], v[98:113]
	v_add_f32_e32 v0, v62, v0
	v_add_f32_e32 v0, v63, v0
	v_add_f32_e32 v0, v64, v0
	v_add_f32_e32 v0, v65, v0
	v_cvt_pk_bf16_f32 v124, v54, v55
	v_cvt_pk_bf16_f32 v125, v56, v57
	s_waitcnt lgkmcnt(2)
	v_mfma_f32_32x32x16_bf16 v[82:97], v[238:241], v[134:137], v[82:97]
	v_cvt_pk_bf16_f32 v126, v58, v59
	v_cvt_pk_bf16_f32 v127, v60, v61
	s_waitcnt lgkmcnt(1)
	v_mfma_f32_32x32x16_bf16 v[98:113], v[242:245], v[130:133], v[98:113]
	v_cvt_pk_bf16_f32 v128, v62, v63
	v_cvt_pk_bf16_f32 v129, v64, v65
	s_waitcnt lgkmcnt(0)
	v_mfma_f32_32x32x16_bf16 v[82:97], v[246:249], v[130:133], v[82:97]
	v_add_f32_e32 v0, v175, v0
	s_setprio 0
	v_max3_f32 v50, v98, v99, v82
	v_max3_f32 v51, v100, v101, v83
	s_nop 0
	v_max3_f32 v50, v50, v84, v85
	v_max3_f32 v51, v51, v104, v105
	s_nop 0
	v_max3_f32 v50, v50, v102, v103
	v_max3_f32 v51, v51, v88, v89
	s_nop 0
	v_max3_f32 v50, v50, v86, v87
	v_max3_f32 v51, v51, v108, v109
	s_nop 0
	v_max3_f32 v50, v50, v106, v107
	v_max3_f32 v51, v51, v92, v93
	s_nop 0
	v_max3_f32 v50, v50, v90, v91
	v_max3_f32 v51, v51, v112, v113
	s_nop 0
	v_max3_f32 v50, v50, v110, v111
	v_max3_f32 v51, v51, v96, v97
	s_nop 0
	v_max3_f32 v50, v50, v94, v95
	v_max_f32_e32 v51, v51, v51
	v_max_f32_e32 v50, v50, v50
	v_max_f32_e32 v50, v50, v51
	v_mov_b32_e32 v51, v50
	s_nop 1
	v_permlane32_swap_b32_e32 v50, v51
	v_max_f32_e32 v51, v51, v51
	v_max_f32_e32 v50, v50, v50
	v_max_f32_e32 v50, v50, v51
	v_cmp_lt_f32_e32 vcc, s54, v50
	s_cmp_lg_u64 vcc, 0
	s_cselect_b64 s[42:43], -1, 0
	s_cbranch_vccnz .LBB0_1117

.LBB0_1114:
	s_or_b64 exec, exec, s[42:43]
	v_lshl_add_u64 v[50:51], v[166:167], 0, s[12:13]
	s_add_i32 s42, s84, s72
	s_mov_b32 s43, m0
	s_mov_b32 m0, s42
	s_nop 0
	global_load_lds_dwordx4 v[50:51], off
	s_mov_b32 m0, s43
	s_mul_i32 s86, s10, 0x3000
	v_add_u32_e32 v184, s86, v173
	s_setprio 1
	ds_read_b128 v[226:229], v184
	ds_read_b128 v[230:233], v184 offset:512
	ds_read_b128 v[234:237], v184 offset:2048
	ds_read_b128 v[238:241], v184 offset:2560
	ds_read_b128 v[242:245], v184 offset:4096
	ds_read_b128 v[246:249], v184 offset:4608
	v_exp_f32_e32 v98, v98
	v_exp_f32_e32 v99, v99
	v_exp_f32_e32 v100, v100
	v_exp_f32_e32 v101, v101
	s_nop 0
	v_exp_f32_e32 v102, v102
	v_exp_f32_e32 v103, v103
	v_exp_f32_e32 v104, v104
	v_exp_f32_e32 v105, v105
	s_waitcnt lgkmcnt(5)
	v_mfma_f32_32x32x16_bf16 v[66:81], v[226:229], v[150:153], v[34:49]
	v_exp_f32_e32 v106, v106
	v_exp_f32_e32 v107, v107
	v_exp_f32_e32 v108, v108
	v_exp_f32_e32 v109, v109
	s_waitcnt lgkmcnt(4)
	v_mfma_f32_32x32x16_bf16 v[50:65], v[230:233], v[150:153], v[34:49]
	ds_read_b128 v[226:229], v184 offset:6144
	ds_read_b128 v[230:233], v184 offset:6656
	v_exp_f32_e32 v110, v110
	v_exp_f32_e32 v111, v111
	v_exp_f32_e32 v112, v112
	v_exp_f32_e32 v113, v113
	s_nop 0
	v_add_f32_e32 v114, 0, v98
	v_add_f32_e32 v114, v99, v114
	v_add_f32_e32 v114, v100, v114
	v_add_f32_e32 v114, v101, v114
	s_waitcnt lgkmcnt(5)
	v_mfma_f32_32x32x16_bf16 v[66:81], v[234:237], v[146:149], v[66:81]
	v_add_f32_e32 v114, v114, v102
	v_add_f32_e32 v114, v103, v114
	v_add_f32_e32 v114, v104, v114
	v_exp_f32_e32 v82, v82
	v_exp_f32_e32 v83, v83
	v_exp_f32_e32 v84, v84
	v_exp_f32_e32 v85, v85
	v_add_f32_e32 v114, v105, v114
	s_waitcnt lgkmcnt(4)
	v_mfma_f32_32x32x16_bf16 v[50:65], v[238:241], v[146:149], v[50:65]
	ds_read_b128 v[234:237], v184 offset:8192
	ds_read_b128 v[238:241], v184 offset:8704
	v_add_f32_e32 v114, v106, v114
	v_add_f32_e32 v114, v107, v114
	v_add_f32_e32 v114, v108, v114
	v_exp_f32_e32 v86, v86
	v_exp_f32_e32 v87, v87
	v_exp_f32_e32 v88, v88
	v_exp_f32_e32 v89, v89
	v_add_f32_e32 v118, v109, v114
	v_cvt_pk_bf16_f32 v114, v98, v99
	v_cvt_pk_bf16_f32 v115, v100, v101
	s_waitcnt lgkmcnt(5)
	v_mfma_f32_32x32x16_bf16 v[66:81], v[242:245], v[142:145], v[66:81]
	v_add_f32_e32 v116, v110, v118
	v_add_f32_e32 v116, v111, v116
	v_add_f32_e32 v116, v112, v116
	v_exp_f32_e32 v90, v90
	v_exp_f32_e32 v91, v91
	v_exp_f32_e32 v92, v92
	v_exp_f32_e32 v93, v93
	v_add_f32_e32 v118, v113, v116
	v_cvt_pk_bf16_f32 v116, v102, v103
	v_cvt_pk_bf16_f32 v117, v104, v105
	s_waitcnt lgkmcnt(4)
	v_mfma_f32_32x32x16_bf16 v[50:65], v[246:249], v[142:145], v[50:65]
	ds_read_b128 v[242:245], v184 offset:10240
	ds_read_b128 v[246:249], v184 offset:10752
	v_exp_f32_e32 v94, v94
	v_exp_f32_e32 v95, v95
	v_exp_f32_e32 v96, v96
	v_exp_f32_e32 v97, v97
	v_cvt_pk_bf16_f32 v119, v108, v109
	v_add_f32_e32 v102, v118, v82
	v_add_f32_e32 v102, v83, v102
	v_add_f32_e32 v102, v84, v102
	v_add_f32_e32 v122, v85, v102
	v_cvt_pk_bf16_f32 v118, v106, v107
	s_waitcnt lgkmcnt(5)
	v_mfma_f32_32x32x16_bf16 v[66:81], v[226:229], v[138:141], v[66:81]
	v_add_f32_e32 v120, v122, v86
	v_add_f32_e32 v120, v87, v120
	v_add_f32_e32 v120, v88, v120
	v_add_f32_e32 v122, v89, v120
	v_cvt_pk_bf16_f32 v120, v110, v111
	v_cvt_pk_bf16_f32 v121, v112, v113
	s_waitcnt lgkmcnt(4)
	v_mfma_f32_32x32x16_bf16 v[50:65], v[230:233], v[138:141], v[50:65]
	v_add_f32_e32 v98, v90, v122
	v_add_f32_e32 v98, v91, v98
	v_add_f32_e32 v98, v92, v98
	v_add_f32_e32 v110, v93, v98
	v_cvt_pk_bf16_f32 v122, v82, v83
	v_cvt_pk_bf16_f32 v123, v84, v85
	s_waitcnt lgkmcnt(3)
	v_mfma_f32_32x32x16_bf16 v[66:81], v[234:237], v[134:137], v[66:81]
	v_add_f32_e32 v110, v94, v110
	v_add_f32_e32 v110, v95, v110
	v_add_f32_e32 v110, v96, v110
	v_add_f32_e32 v110, v97, v110
	v_cvt_pk_bf16_f32 v124, v86, v87
	v_cvt_pk_bf16_f32 v125, v88, v89
	s_waitcnt lgkmcnt(2)
	v_mfma_f32_32x32x16_bf16 v[50:65], v[238:241], v[134:137], v[50:65]
	v_cvt_pk_bf16_f32 v126, v90, v91
	v_cvt_pk_bf16_f32 v127, v92, v93
	s_waitcnt lgkmcnt(1)
	v_mfma_f32_32x32x16_bf16 v[66:81], v[242:245], v[130:133], v[66:81]
	v_cvt_pk_bf16_f32 v128, v94, v95
	v_cvt_pk_bf16_f32 v129, v96, v97
	s_waitcnt lgkmcnt(0)
	v_mfma_f32_32x32x16_bf16 v[50:65], v[246:249], v[130:133], v[50:65]
	v_add_f32_e32 v175, v0, v110
	s_setprio 0
	v_max3_f32 v0, v66, v67, v50
	v_max3_f32 v82, v68, v69, v51
	s_nop 0
	v_max3_f32 v0, v0, v52, v53
	v_max3_f32 v82, v82, v72, v73
	s_nop 0
	v_max3_f32 v0, v0, v70, v71
	v_max3_f32 v82, v82, v56, v57
	s_nop 0
	v_max3_f32 v0, v0, v54, v55
	v_max3_f32 v82, v82, v76, v77
	s_nop 0
	v_max3_f32 v0, v0, v74, v75
	v_max3_f32 v82, v82, v60, v61
	s_nop 0
	v_max3_f32 v0, v0, v58, v59
	v_max3_f32 v82, v82, v80, v81
	s_nop 0
	v_max3_f32 v0, v0, v78, v79
	v_max3_f32 v82, v82, v64, v65
	s_nop 0
	v_max3_f32 v0, v0, v62, v63
	v_max_f32_e32 v82, v82, v82
	v_max_f32_e32 v0, v0, v0
	v_max_f32_e32 v0, v0, v82
	v_mov_b32_e32 v82, v0
	s_nop 1
	v_permlane32_swap_b32_e32 v0, v82
	v_max_f32_e32 v82, v82, v82
	v_max_f32_e32 v0, v0, v0
	v_max_f32_e32 v0, v0, v82
	v_cmp_lt_f32_e32 vcc, s54, v0
	s_cmp_lg_u64 vcc, 0
	s_cselect_b64 s[42:43], -1, 0
	s_cbranch_vccnz .LBB0_1120

.LBB0_1128:
	s_or_b64 exec, exec, s[44:45]
	v_lshl_add_u64 v[82:83], v[156:157], 0, s[0:1]
	s_add_i32 s0, s85, s72
	s_mov_b32 s1, m0
	s_mov_b32 m0, s0
	s_nop 0
	global_load_lds_dwordx4 v[82:83], off
	s_mov_b32 m0, s1
	v_or_b32_e32 v182, s75, v169
	v_add_u32_e32 v183, s77, v173
	s_setprio 1
	ds_read_b128 v[226:229], v183
	ds_read_b128 v[230:233], v183 offset:512
	ds_read_b128 v[234:237], v183 offset:2048
	ds_read_b128 v[238:241], v183 offset:2560
	ds_read_b128 v[242:245], v183 offset:4096
	ds_read_b128 v[246:249], v183 offset:4608
	v_exp_f32_e32 v66, v66
	v_exp_f32_e32 v67, v67
	v_exp_f32_e32 v68, v68
	v_exp_f32_e32 v69, v69
	s_nop 0
	v_exp_f32_e32 v70, v70
	v_exp_f32_e32 v71, v71
	v_exp_f32_e32 v72, v72
	v_exp_f32_e32 v73, v73
	s_waitcnt lgkmcnt(5)
	v_mfma_f32_32x32x16_bf16 v[82:97], v[226:229], v[150:153], v[34:49]
	v_exp_f32_e32 v74, v74
	v_exp_f32_e32 v75, v75
	v_exp_f32_e32 v76, v76
	v_exp_f32_e32 v77, v77
	s_nop 0
	v_exp_f32_e32 v78, v78
	v_exp_f32_e32 v79, v79
	v_exp_f32_e32 v80, v80
	v_exp_f32_e32 v81, v81
	s_waitcnt lgkmcnt(4)
	v_mfma_f32_32x32x16_bf16 v[98:113], v[230:233], v[150:153], v[34:49]
	ds_read_b128 v[226:229], v183 offset:6144
	ds_read_b128 v[230:233], v183 offset:6656
	v_add_f32_e32 v0, 0, v66
	v_add_f32_e32 v0, v67, v0
	v_add_f32_e32 v0, v68, v0
	v_add_f32_e32 v0, v69, v0
	s_waitcnt lgkmcnt(5)
	v_mfma_f32_32x32x16_bf16 v[82:97], v[234:237], v[146:149], v[82:97]
	v_add_f32_e32 v0, v0, v70
	v_add_f32_e32 v0, v71, v0
	v_add_f32_e32 v0, v72, v0
	v_exp_f32_e32 v50, v50
	v_exp_f32_e32 v51, v51
	v_exp_f32_e32 v52, v52
	v_exp_f32_e32 v53, v53
	v_add_f32_e32 v0, v73, v0
	s_nop 0
	v_add_f32_e32 v0, v74, v0
	v_add_f32_e32 v0, v75, v0
	v_add_f32_e32 v0, v76, v0
	v_exp_f32_e32 v54, v54
	v_exp_f32_e32 v55, v55
	v_exp_f32_e32 v56, v56
	v_exp_f32_e32 v57, v57
	v_add_f32_e32 v0, v77, v0
	v_cvt_pk_bf16_f32 v114, v66, v67
	v_cvt_pk_bf16_f32 v115, v68, v69
	s_waitcnt lgkmcnt(4)
	v_mfma_f32_32x32x16_bf16 v[98:113], v[238:241], v[146:149], v[98:113]
	ds_read_b128 v[234:237], v183 offset:8192
	ds_read_b128 v[238:241], v183 offset:8704
	s_waitcnt lgkmcnt(5)
	v_mfma_f32_32x32x16_bf16 v[82:97], v[242:245], v[142:145], v[82:97]
	v_add_f32_e32 v0, v78, v0
	v_add_f32_e32 v0, v79, v0
	v_add_f32_e32 v0, v80, v0
	v_exp_f32_e32 v58, v58
	v_exp_f32_e32 v59, v59
	v_exp_f32_e32 v60, v60
	v_exp_f32_e32 v61, v61
	v_add_f32_e32 v0, v81, v0
	v_cvt_pk_bf16_f32 v116, v70, v71
	v_cvt_pk_bf16_f32 v117, v72, v73
	s_nop 0
	v_exp_f32_e32 v62, v62
	v_exp_f32_e32 v63, v63
	v_exp_f32_e32 v64, v64
	v_exp_f32_e32 v65, v65
	v_cvt_pk_bf16_f32 v118, v74, v75
	v_add_f32_e32 v0, v0, v50
	v_add_f32_e32 v0, v51, v0
	v_add_f32_e32 v0, v52, v0
	v_add_f32_e32 v0, v53, v0
	v_cvt_pk_bf16_f32 v119, v76, v77
	s_waitcnt lgkmcnt(4)
	v_mfma_f32_32x32x16_bf16 v[98:113], v[246:249], v[142:145], v[98:113]
	ds_read_b128 v[242:245], v183 offset:10240
	ds_read_b128 v[246:249], v183 offset:10752
	s_waitcnt lgkmcnt(5)
	v_mfma_f32_32x32x16_bf16 v[82:97], v[226:229], v[138:141], v[82:97]
	v_add_f32_e32 v0, v0, v54
	v_add_f32_e32 v0, v55, v0
	v_add_f32_e32 v0, v56, v0
	v_add_f32_e32 v0, v57, v0
	v_cvt_pk_bf16_f32 v120, v78, v79
	v_cvt_pk_bf16_f32 v121, v80, v81
	s_nop 0
	v_add_f32_e32 v0, v58, v0
	v_add_f32_e32 v0, v59, v0
	v_add_f32_e32 v0, v60, v0
	v_add_f32_e32 v0, v61, v0
	v_cvt_pk_bf16_f32 v122, v50, v51
	v_cvt_pk_bf16_f32 v123, v52, v53
	s_waitcnt lgkmcnt(4)
	v_mfma_f32_32x32x16_bf16 v[98:113], v[230:233], v[138:141], v[98:113]
	s_waitcnt lgkmcnt(3)
	v_mfma_f32_32x32x16_bf16 v[82:97], v[234:237], v[134:137], v[82:97]
	v_add_f32_e32 v0, v62, v0
	v_add_f32_e32 v0, v63, v0
	v_add_f32_e32 v0, v64, v0
	v_add_f32_e32 v0, v65, v0
	v_cvt_pk_bf16_f32 v124, v54, v55
	v_cvt_pk_bf16_f32 v125, v56, v57
	v_cvt_pk_bf16_f32 v126, v58, v59
	v_cvt_pk_bf16_f32 v127, v60, v61
	s_waitcnt lgkmcnt(2)
	v_mfma_f32_32x32x16_bf16 v[98:113], v[238:241], v[134:137], v[98:113]
	s_waitcnt lgkmcnt(1)
	v_mfma_f32_32x32x16_bf16 v[82:97], v[242:245], v[130:133], v[82:97]
	v_cvt_pk_bf16_f32 v128, v62, v63
	v_cvt_pk_bf16_f32 v129, v64, v65
	s_waitcnt lgkmcnt(0)
; __device__ __forceinline__ float max3f(float a, float b, float c) { float r; asm("v_max3_f32 %0, %1, %2, %3" : "=v"(r) : "v"(a), "v"(b), "v"(c)); return r; }
; __device__ __forceinline__ void cmask(f32x16& p0, f32x16& p1, int jb, int qrel, int hi) {
;     const float NEG = -INFINITY; const int kb = 64 * jb + 4 * hi;
; #pragma unroll
;     for (int r = 0; r < 16; ++r) { const int kv = kb + (r & 3) + 8 * (r >> 2); if (kv > qrel) p0[r] = NEG; if (kv + 32 > qrel) p1[r] = NEG; }
; }
; __device__ __forceinline__ float rowmax(const f32x16& p0, const f32x16& p1) {
;     float a = max3f(p0[0], p0[1], p1[0]), b = max3f(p0[2], p0[3], p1[1]); a = max3f(a, p1[2], p1[3]);
; #pragma unroll
;     for (int r = 4; r < 16; r += 4) { a = max3f(a, p0[r], p0[r + 1]); b = max3f(b, p0[r + 2], p0[r + 3]); a = max3f(a, p1[r], p1[r + 1]); b = max3f(b, p1[r + 2], p1[r + 3]); }
;     const float m = fmaxf(a, b);
;     auto rr = __builtin_amdgcn_permlane32_swap(__float_as_uint(m), __float_as_uint(m), false, false);
;     return fmaxf(__uint_as_float(rr[0]), __uint_as_float(rr[1]));
; }
	v_mfma_f32_32x32x16_bf16 v[98:113], v[246:249], v[130:133], v[98:113]
	v_add_f32_e32 v187, v175, v0
	s_setprio 0
	v_lshlrev_b32_e32 v186, 2, v170
	v_or_b32_e32 v0, 32, v186
	v_cmp_le_i32_e32 vcc, v0, v182
	v_or_b32_e32 v0, 33, v186
	v_or_b32_e32 v179, 2, v186
	s_nop 4
	v_cndmask_b32_e32 v50, v206, v98, vcc
	v_cmp_lt_i32_e32 vcc, v186, v182
	v_or_b32_e32 v178, 3, v186
	v_or_b32_e32 v177, 8, v186
	v_cndmask_b32_e32 v67, v206, v83, vcc
	v_cmp_le_i32_e32 vcc, v186, v182
	v_or_b32_e32 v176, 9, v186
	v_or_b32_e32 v175, 10, v186
	v_cndmask_b32_e32 v66, v206, v82, vcc
	v_cmp_le_i32_e32 vcc, v0, v182
	v_or_b32_e32 v0, 34, v186
	v_or_b32_e32 v174, 11, v186
	v_cndmask_b32_e32 v51, v206, v99, vcc
	v_cmp_le_i32_e32 vcc, v179, v182
	v_or_b32_e32 v173, 16, v186
	v_or_b32_e32 v167, 17, v186
	v_cndmask_b32_e32 v68, v206, v84, vcc
	v_cmp_le_i32_e32 vcc, v0, v182
	v_or_b32_e32 v0, 35, v186
	v_or_b32_e32 v166, 18, v186
	v_cndmask_b32_e32 v52, v206, v100, vcc
	v_cmp_le_i32_e32 vcc, v178, v182
	v_or_b32_e32 v165, 19, v186
	v_or_b32_e32 v164, 24, v186
	v_cndmask_b32_e32 v69, v206, v85, vcc
	v_cmp_le_i32_e32 vcc, v0, v182
	v_or_b32_e32 v0, 40, v186
	v_or_b32_e32 v163, 25, v186
	v_cndmask_b32_e32 v53, v206, v101, vcc
	v_cmp_le_i32_e32 vcc, v177, v182
	v_max3_f32 v82, v66, v67, v50
	v_max3_f32 v83, v68, v69, v51
	v_or_b32_e32 v162, 26, v186
	v_max3_f32 v82, v82, v52, v53
	v_or_b32_e32 v65, 59, v186
	v_cndmask_b32_e32 v70, v206, v86, vcc
	v_cmp_le_i32_e32 vcc, v0, v182
	v_or_b32_e32 v0, 41, v186
	s_nop 0
	v_cndmask_b32_e32 v54, v206, v102, vcc
	v_cmp_le_i32_e32 vcc, v176, v182
	s_nop 1
	v_cndmask_b32_e32 v71, v206, v87, vcc
	v_cmp_le_i32_e32 vcc, v0, v182
	v_or_b32_e32 v0, 42, v186
	v_max3_f32 v82, v82, v70, v71
	s_nop 0
	v_cndmask_b32_e32 v55, v206, v103, vcc
	v_cmp_le_i32_e32 vcc, v175, v182
	v_max3_f32 v82, v82, v54, v55
	s_nop 1
	v_cndmask_b32_e32 v72, v206, v88, vcc
	v_cmp_le_i32_e32 vcc, v0, v182
	v_or_b32_e32 v0, 43, v186
	s_nop 0
	v_cndmask_b32_e32 v56, v206, v104, vcc
	v_cmp_le_i32_e32 vcc, v174, v182
	s_nop 1
	v_cndmask_b32_e32 v73, v206, v89, vcc
	v_cmp_le_i32_e32 vcc, v0, v182
	v_or_b32_e32 v0, 48, v186
	v_max3_f32 v83, v83, v72, v73
	s_nop 0
	v_cndmask_b32_e32 v57, v206, v105, vcc
	v_cmp_le_i32_e32 vcc, v173, v182
	v_max3_f32 v83, v83, v56, v57
	s_nop 1
	v_cndmask_b32_e32 v74, v206, v90, vcc
	v_cmp_le_i32_e32 vcc, v0, v182
	v_or_b32_e32 v0, 49, v186
	s_nop 0
	v_cndmask_b32_e32 v58, v206, v106, vcc
	v_cmp_le_i32_e32 vcc, v167, v182
	s_nop 1
	v_cndmask_b32_e32 v75, v206, v91, vcc
	v_cmp_le_i32_e32 vcc, v0, v182
	v_or_b32_e32 v0, 50, v186
	v_max3_f32 v82, v82, v74, v75
	s_nop 0
	v_cndmask_b32_e32 v59, v206, v107, vcc
	v_cmp_le_i32_e32 vcc, v166, v182
	v_max3_f32 v82, v82, v58, v59
	s_nop 1
	v_cndmask_b32_e32 v76, v206, v92, vcc
	v_cmp_le_i32_e32 vcc, v0, v182
	v_or_b32_e32 v0, 51, v186
	s_nop 0
	v_cndmask_b32_e32 v60, v206, v108, vcc
	v_cmp_le_i32_e32 vcc, v165, v182
	s_nop 1
	v_cndmask_b32_e32 v77, v206, v93, vcc
	v_cmp_le_i32_e32 vcc, v0, v182
	v_or_b32_e32 v0, 56, v186
	v_max3_f32 v83, v83, v76, v77
	s_nop 0
	v_cndmask_b32_e32 v61, v206, v109, vcc
	v_cmp_le_i32_e32 vcc, v164, v182
	v_max3_f32 v83, v83, v60, v61
	s_nop 1
	v_cndmask_b32_e32 v78, v206, v94, vcc
	v_cmp_le_i32_e32 vcc, v0, v182
	v_or_b32_e32 v0, 57, v186
	s_nop 0
	v_cndmask_b32_e32 v62, v206, v110, vcc
	v_cmp_le_i32_e32 vcc, v163, v182
	s_nop 1
	v_cndmask_b32_e32 v79, v206, v95, vcc
	v_cmp_le_i32_e32 vcc, v0, v182
	v_or_b32_e32 v0, 58, v186
	v_max3_f32 v82, v82, v78, v79
	s_nop 0
	v_cndmask_b32_e32 v63, v206, v111, vcc
	v_cmp_le_i32_e32 vcc, v162, v182
	v_max3_f32 v82, v82, v62, v63
	s_nop 0
	v_max_f32_e32 v82, v82, v82
	v_cndmask_b32_e32 v80, v206, v96, vcc
	v_cmp_le_i32_e32 vcc, v0, v182
	v_or_b32_e32 v0, 27, v186
	s_nop 0
	v_cndmask_b32_e32 v64, v206, v112, vcc
	v_cmp_le_i32_e32 vcc, v0, v182
	s_nop 1
	v_cndmask_b32_e32 v81, v206, v97, vcc
	v_cmp_le_i32_e32 vcc, v65, v182
	v_max3_f32 v83, v83, v80, v81
	s_nop 1
	v_cndmask_b32_e32 v65, v206, v113, vcc
	v_max3_f32 v83, v83, v64, v65
	s_nop 0
	v_max_f32_e32 v83, v83, v83
	v_max_f32_e32 v82, v82, v83
	v_mov_b32_e32 v83, v82
	s_nop 1
	v_permlane32_swap_b32_e32 v82, v83
	v_max_f32_e32 v83, v83, v83
	v_max_f32_e32 v82, v82, v82
	v_max_f32_e32 v82, v82, v83
	v_cmp_lt_f32_e32 vcc, s54, v82
	s_cmp_lg_u64 vcc, 0
	s_cselect_b64 s[0:1], -1, 0
	s_cbranch_vccnz .LBB0_1208

.LBB0_1133:
	s_or_b64 exec, exec, s[44:45]
	v_lshl_add_u64 v[82:83], v[156:157], 0, s[42:43]
	s_add_i32 s10, s79, s72
	s_mov_b32 s42, m0
	s_mov_b32 m0, s10
	s_nop 0
	global_load_lds_dwordx4 v[82:83], off
	s_mov_b32 m0, s42
	s_setprio 1
	ds_read_b128 v[226:229], v185
	ds_read_b128 v[230:233], v185 offset:512
	ds_read_b128 v[234:237], v185 offset:2048
	ds_read_b128 v[238:241], v185 offset:2560
	ds_read_b128 v[242:245], v185 offset:4096
	ds_read_b128 v[246:249], v185 offset:4608
	v_exp_f32_e32 v66, v66
	v_exp_f32_e32 v67, v67
	v_exp_f32_e32 v68, v68
	v_exp_f32_e32 v69, v69
	s_nop 0
	v_exp_f32_e32 v70, v70
	v_exp_f32_e32 v71, v71
	v_exp_f32_e32 v72, v72
	v_exp_f32_e32 v73, v73
	s_waitcnt lgkmcnt(5)
	v_mfma_f32_32x32x16_bf16 v[82:97], v[226:229], v[150:153], v[34:49]
	v_exp_f32_e32 v74, v74
	v_exp_f32_e32 v75, v75
	v_exp_f32_e32 v76, v76
	v_exp_f32_e32 v77, v77
	s_nop 0
	v_exp_f32_e32 v78, v78
	v_exp_f32_e32 v79, v79
	v_exp_f32_e32 v80, v80
	v_exp_f32_e32 v81, v81
	s_waitcnt lgkmcnt(4)
	v_mfma_f32_32x32x16_bf16 v[98:113], v[230:233], v[150:153], v[34:49]
	ds_read_b128 v[226:229], v185 offset:6144
	ds_read_b128 v[230:233], v185 offset:6656
	v_add_f32_e32 v114, 0, v66
	v_add_f32_e32 v114, v67, v114
	v_add_f32_e32 v114, v68, v114
	v_add_f32_e32 v114, v69, v114
	s_waitcnt lgkmcnt(5)
	v_mfma_f32_32x32x16_bf16 v[82:97], v[234:237], v[146:149], v[82:97]
	v_add_f32_e32 v114, v114, v70
	v_add_f32_e32 v114, v71, v114
	v_add_f32_e32 v114, v72, v114
	v_exp_f32_e32 v50, v50
	v_exp_f32_e32 v51, v51
	v_exp_f32_e32 v52, v52
	v_exp_f32_e32 v53, v53
	v_add_f32_e32 v114, v73, v114
	s_nop 0
	v_add_f32_e32 v114, v74, v114
	v_add_f32_e32 v114, v75, v114
	v_add_f32_e32 v114, v76, v114
	v_exp_f32_e32 v54, v54
	v_exp_f32_e32 v55, v55
	v_exp_f32_e32 v56, v56
	v_exp_f32_e32 v57, v57
	v_add_f32_e32 v118, v77, v114
	v_cvt_pk_bf16_f32 v114, v66, v67
	v_cvt_pk_bf16_f32 v115, v68, v69
	s_waitcnt lgkmcnt(4)
	v_mfma_f32_32x32x16_bf16 v[98:113], v[238:241], v[146:149], v[98:113]
	ds_read_b128 v[234:237], v185 offset:8192
	ds_read_b128 v[238:241], v185 offset:8704
	s_waitcnt lgkmcnt(5)
	v_mfma_f32_32x32x16_bf16 v[82:97], v[242:245], v[142:145], v[82:97]
	v_add_f32_e32 v116, v78, v118
	v_add_f32_e32 v116, v79, v116
	v_add_f32_e32 v116, v80, v116
	v_exp_f32_e32 v58, v58
	v_exp_f32_e32 v59, v59
	v_exp_f32_e32 v60, v60
	v_exp_f32_e32 v61, v61
	v_add_f32_e32 v118, v81, v116
	v_cvt_pk_bf16_f32 v116, v70, v71
	v_cvt_pk_bf16_f32 v117, v72, v73
	s_nop 0
	v_exp_f32_e32 v62, v62
	v_exp_f32_e32 v63, v63
	v_exp_f32_e32 v64, v64
	v_exp_f32_e32 v65, v65
	v_cvt_pk_bf16_f32 v119, v76, v77
	v_add_f32_e32 v70, v118, v50
	v_add_f32_e32 v70, v51, v70
	v_add_f32_e32 v70, v52, v70
	v_add_f32_e32 v122, v53, v70
	v_cvt_pk_bf16_f32 v118, v74, v75
	s_waitcnt lgkmcnt(4)
	v_mfma_f32_32x32x16_bf16 v[98:113], v[246:249], v[142:145], v[98:113]
	ds_read_b128 v[242:245], v185 offset:10240
	ds_read_b128 v[246:249], v185 offset:10752
	s_waitcnt lgkmcnt(5)
	v_mfma_f32_32x32x16_bf16 v[82:97], v[226:229], v[138:141], v[82:97]
	v_add_f32_e32 v120, v122, v54
	v_add_f32_e32 v120, v55, v120
	v_add_f32_e32 v120, v56, v120
	v_add_f32_e32 v122, v57, v120
	v_cvt_pk_bf16_f32 v120, v78, v79
	v_cvt_pk_bf16_f32 v121, v80, v81
	s_nop 0
	v_add_f32_e32 v66, v58, v122
	v_add_f32_e32 v66, v59, v66
	v_add_f32_e32 v66, v60, v66
	v_add_f32_e32 v78, v61, v66
	v_cvt_pk_bf16_f32 v122, v50, v51
	v_cvt_pk_bf16_f32 v123, v52, v53
	s_waitcnt lgkmcnt(4)
	v_mfma_f32_32x32x16_bf16 v[98:113], v[230:233], v[138:141], v[98:113]
	s_waitcnt lgkmcnt(3)
	v_mfma_f32_32x32x16_bf16 v[82:97], v[234:237], v[134:137], v[82:97]
	v_add_f32_e32 v78, v62, v78
	v_add_f32_e32 v78, v63, v78
	v_add_f32_e32 v78, v64, v78
	v_add_f32_e32 v78, v65, v78
	v_cvt_pk_bf16_f32 v124, v54, v55
	v_cvt_pk_bf16_f32 v125, v56, v57
	v_cvt_pk_bf16_f32 v126, v58, v59
	v_cvt_pk_bf16_f32 v127, v60, v61
	s_waitcnt lgkmcnt(2)
	v_mfma_f32_32x32x16_bf16 v[98:113], v[238:241], v[134:137], v[98:113]
	s_waitcnt lgkmcnt(1)
	v_mfma_f32_32x32x16_bf16 v[82:97], v[242:245], v[130:133], v[82:97]
	v_cvt_pk_bf16_f32 v128, v62, v63
	v_cvt_pk_bf16_f32 v129, v64, v65
	s_waitcnt lgkmcnt(0)
; __device__ __forceinline__ float max3f(float a, float b, float c) { float r; asm("v_max3_f32 %0, %1, %2, %3" : "=v"(r) : "v"(a), "v"(b), "v"(c)); return r; }
; __device__ __forceinline__ void cmask(f32x16& p0, f32x16& p1, int jb, int qrel, int hi) {
;     const float NEG = -INFINITY; const int kb = 64 * jb + 4 * hi;
; #pragma unroll
;     for (int r = 0; r < 16; ++r) { const int kv = kb + (r & 3) + 8 * (r >> 2); if (kv > qrel) p0[r] = NEG; if (kv + 32 > qrel) p1[r] = NEG; }
; }
; __device__ __forceinline__ float rowmax(const f32x16& p0, const f32x16& p1) {
;     float a = max3f(p0[0], p0[1], p1[0]), b = max3f(p0[2], p0[3], p1[1]); a = max3f(a, p1[2], p1[3]);
; #pragma unroll
;     for (int r = 4; r < 16; r += 4) { a = max3f(a, p0[r], p0[r + 1]); b = max3f(b, p0[r + 2], p0[r + 3]); a = max3f(a, p1[r], p1[r + 1]); b = max3f(b, p1[r + 2], p1[r + 3]); }
;     const float m = fmaxf(a, b);
;     auto rr = __builtin_amdgcn_permlane32_swap(__float_as_uint(m), __float_as_uint(m), false, false);
;     return fmaxf(__uint_as_float(rr[0]), __uint_as_float(rr[1]));
; }
	v_mfma_f32_32x32x16_bf16 v[98:113], v[246:249], v[130:133], v[98:113]
	v_add_f32_e32 v158, v187, v78
	s_setprio 0
	v_or_b32_e32 v50, 0x60, v186
	v_or_b32_e32 v51, 64, v186
	v_cmp_le_i32_e32 vcc, v50, v182
	v_or_b32_e32 v52, 0x42, v186
	v_or_b32_e32 v53, 0x43, v186
	s_nop 4
	v_cndmask_b32_e32 v50, v206, v98, vcc
	v_cmp_lt_i32_e32 vcc, v51, v182
	v_or_b32_e32 v54, 0x48, v186
	v_or_b32_e32 v55, 0x49, v186
	v_cndmask_b32_e32 v67, v206, v83, vcc
	v_cmp_le_i32_e32 vcc, v51, v182
	v_or_b32_e32 v51, 0x61, v186
	v_or_b32_e32 v56, 0x4a, v186
	v_cndmask_b32_e32 v66, v206, v82, vcc
	v_cmp_le_i32_e32 vcc, v51, v182
	v_or_b32_e32 v57, 0x4b, v186
	v_or_b32_e32 v58, 0x50, v186
	v_cndmask_b32_e32 v51, v206, v99, vcc
	v_cmp_le_i32_e32 vcc, v52, v182
	v_or_b32_e32 v52, 0x62, v186
	v_or_b32_e32 v59, 0x51, v186
	v_cndmask_b32_e32 v68, v206, v84, vcc
	v_cmp_le_i32_e32 vcc, v52, v182
	v_or_b32_e32 v60, 0x52, v186
	v_or_b32_e32 v61, 0x53, v186
	v_cndmask_b32_e32 v52, v206, v100, vcc
	v_cmp_le_i32_e32 vcc, v53, v182
	v_or_b32_e32 v53, 0x63, v186
	v_or_b32_e32 v62, 0x58, v186
	v_cndmask_b32_e32 v69, v206, v85, vcc
	v_cmp_le_i32_e32 vcc, v53, v182
	v_or_b32_e32 v63, 0x59, v186
	v_max3_f32 v82, v66, v67, v50
	v_max3_f32 v83, v68, v69, v51
	v_or_b32_e32 v64, 0x5a, v186
	v_cndmask_b32_e32 v53, v206, v101, vcc
	v_cmp_le_i32_e32 vcc, v54, v182
	v_or_b32_e32 v54, 0x68, v186
	v_max3_f32 v82, v82, v52, v53
	v_or_b32_e32 v65, 0x5b, v186
	v_cndmask_b32_e32 v70, v206, v86, vcc
	v_cmp_le_i32_e32 vcc, v54, v182
	s_nop 1
	v_cndmask_b32_e32 v54, v206, v102, vcc
	v_cmp_le_i32_e32 vcc, v55, v182
	v_or_b32_e32 v55, 0x69, v186
	s_nop 0
	v_cndmask_b32_e32 v71, v206, v87, vcc
	v_cmp_le_i32_e32 vcc, v55, v182
	v_max3_f32 v82, v82, v70, v71
	s_nop 1
	v_cndmask_b32_e32 v55, v206, v103, vcc
	v_cmp_le_i32_e32 vcc, v56, v182
	v_or_b32_e32 v56, 0x6a, v186
	v_max3_f32 v82, v82, v54, v55
	s_nop 0
	v_cndmask_b32_e32 v72, v206, v88, vcc
	v_cmp_le_i32_e32 vcc, v56, v182
	s_nop 1
	v_cndmask_b32_e32 v56, v206, v104, vcc
	v_cmp_le_i32_e32 vcc, v57, v182
	v_or_b32_e32 v57, 0x6b, v186
	s_nop 0
	v_cndmask_b32_e32 v73, v206, v89, vcc
	v_cmp_le_i32_e32 vcc, v57, v182
	v_max3_f32 v83, v83, v72, v73
	s_nop 1
	v_cndmask_b32_e32 v57, v206, v105, vcc
	v_cmp_le_i32_e32 vcc, v58, v182
	v_or_b32_e32 v58, 0x70, v186
	v_max3_f32 v83, v83, v56, v57
	s_nop 0
	v_cndmask_b32_e32 v74, v206, v90, vcc
	v_cmp_le_i32_e32 vcc, v58, v182
	s_nop 1
	v_cndmask_b32_e32 v58, v206, v106, vcc
	v_cmp_le_i32_e32 vcc, v59, v182
	v_or_b32_e32 v59, 0x71, v186
	s_nop 0
	v_cndmask_b32_e32 v75, v206, v91, vcc
	v_cmp_le_i32_e32 vcc, v59, v182
	v_max3_f32 v82, v82, v74, v75
	s_nop 1
	v_cndmask_b32_e32 v59, v206, v107, vcc
	v_cmp_le_i32_e32 vcc, v60, v182
	v_or_b32_e32 v60, 0x72, v186
	v_max3_f32 v82, v82, v58, v59
	s_nop 0
	v_cndmask_b32_e32 v76, v206, v92, vcc
	v_cmp_le_i32_e32 vcc, v60, v182
	s_nop 1
	v_cndmask_b32_e32 v60, v206, v108, vcc
	v_cmp_le_i32_e32 vcc, v61, v182
	v_or_b32_e32 v61, 0x73, v186
	s_nop 0
	v_cndmask_b32_e32 v77, v206, v93, vcc
	v_cmp_le_i32_e32 vcc, v61, v182
	v_max3_f32 v83, v83, v76, v77
	s_nop 1
	v_cndmask_b32_e32 v61, v206, v109, vcc
	v_cmp_le_i32_e32 vcc, v62, v182
	v_or_b32_e32 v62, 0x78, v186
	v_max3_f32 v83, v83, v60, v61
	s_nop 0
	v_cndmask_b32_e32 v78, v206, v94, vcc
	v_cmp_le_i32_e32 vcc, v62, v182
	s_nop 1
	v_cndmask_b32_e32 v62, v206, v110, vcc
	v_cmp_le_i32_e32 vcc, v63, v182
	v_or_b32_e32 v63, 0x79, v186
	s_nop 0
	v_cndmask_b32_e32 v79, v206, v95, vcc
	v_cmp_le_i32_e32 vcc, v63, v182
	v_max3_f32 v82, v82, v78, v79
	s_nop 1
	v_cndmask_b32_e32 v63, v206, v111, vcc
	v_cmp_le_i32_e32 vcc, v64, v182
	v_or_b32_e32 v64, 0x7a, v186
	v_max3_f32 v82, v82, v62, v63
	s_nop 0
	v_cndmask_b32_e32 v80, v206, v96, vcc
	v_cmp_le_i32_e32 vcc, v64, v182
	v_max_f32_e32 v82, v82, v82
	s_nop 0
	v_cndmask_b32_e32 v64, v206, v112, vcc
	v_cmp_le_i32_e32 vcc, v65, v182
	v_or_b32_e32 v65, 0x7b, v186
	s_nop 0
	v_cndmask_b32_e32 v81, v206, v97, vcc
	v_cmp_le_i32_e32 vcc, v65, v182
	v_max3_f32 v83, v83, v80, v81
	s_nop 1
	v_cndmask_b32_e32 v65, v206, v113, vcc
	v_max3_f32 v83, v83, v64, v65
	s_nop 0
	v_max_f32_e32 v83, v83, v83
	v_max_f32_e32 v82, v82, v83
	v_mov_b32_e32 v83, v82
	s_nop 1
	v_permlane32_swap_b32_e32 v82, v83
	v_max_f32_e32 v83, v83, v83
	v_max_f32_e32 v82, v82, v82
	v_max_f32_e32 v82, v82, v83
	v_cmp_lt_f32_e32 vcc, s54, v82
	s_cmp_lg_u64 vcc, 0
	s_cselect_b64 s[42:43], -1, 0
	s_cbranch_vccnz .LBB0_1211

.LBB0_1136:
	v_lshl_add_u64 v[82:83], v[156:157], 0, s[0:1]
	s_mov_b32 s0, m0
	s_mov_b32 m0, s73
	s_nop 0
	global_load_lds_dwordx4 v[82:83], off
	s_mov_b32 m0, s0
	s_setprio 1
	ds_read_b128 v[226:229], v184
	ds_read_b128 v[230:233], v184 offset:512
	ds_read_b128 v[234:237], v184 offset:2048
	ds_read_b128 v[238:241], v184 offset:2560
	ds_read_b128 v[242:245], v184 offset:4096
	ds_read_b128 v[246:249], v184 offset:4608
	v_exp_f32_e32 v66, v66
	v_exp_f32_e32 v67, v67
	v_exp_f32_e32 v68, v68
	v_exp_f32_e32 v69, v69
	s_nop 0
	v_exp_f32_e32 v70, v70
	v_exp_f32_e32 v71, v71
	v_exp_f32_e32 v72, v72
	v_exp_f32_e32 v73, v73
	s_waitcnt lgkmcnt(5)
	v_mfma_f32_32x32x16_bf16 v[82:97], v[226:229], v[150:153], v[34:49]
	v_exp_f32_e32 v74, v74
	v_exp_f32_e32 v75, v75
	v_exp_f32_e32 v76, v76
	v_exp_f32_e32 v77, v77
	s_nop 0
	v_exp_f32_e32 v78, v78
	v_exp_f32_e32 v79, v79
	v_exp_f32_e32 v80, v80
	v_exp_f32_e32 v81, v81
	s_waitcnt lgkmcnt(4)
	v_mfma_f32_32x32x16_bf16 v[98:113], v[230:233], v[150:153], v[34:49]
	ds_read_b128 v[226:229], v184 offset:6144
	ds_read_b128 v[230:233], v184 offset:6656
	v_add_f32_e32 v114, 0, v66
	v_add_f32_e32 v114, v67, v114
	v_add_f32_e32 v114, v68, v114
	v_add_f32_e32 v114, v69, v114
	s_waitcnt lgkmcnt(5)
	v_mfma_f32_32x32x16_bf16 v[82:97], v[234:237], v[146:149], v[82:97]
	v_add_f32_e32 v114, v114, v70
	v_add_f32_e32 v114, v71, v114
	v_add_f32_e32 v114, v72, v114
	v_exp_f32_e32 v50, v50
	v_exp_f32_e32 v51, v51
	v_exp_f32_e32 v52, v52
	v_exp_f32_e32 v53, v53
	v_add_f32_e32 v114, v73, v114
	s_nop 0
	v_add_f32_e32 v114, v74, v114
	v_add_f32_e32 v114, v75, v114
	v_add_f32_e32 v114, v76, v114
	v_exp_f32_e32 v54, v54
	v_exp_f32_e32 v55, v55
	v_exp_f32_e32 v56, v56
	v_exp_f32_e32 v57, v57
	v_add_f32_e32 v118, v77, v114
	v_cvt_pk_bf16_f32 v114, v66, v67
	v_cvt_pk_bf16_f32 v115, v68, v69
	s_waitcnt lgkmcnt(4)
	v_mfma_f32_32x32x16_bf16 v[98:113], v[238:241], v[146:149], v[98:113]
	ds_read_b128 v[234:237], v184 offset:8192
	ds_read_b128 v[238:241], v184 offset:8704
	s_waitcnt lgkmcnt(5)
	v_mfma_f32_32x32x16_bf16 v[82:97], v[242:245], v[142:145], v[82:97]
	v_add_f32_e32 v116, v78, v118
	v_add_f32_e32 v116, v79, v116
	v_add_f32_e32 v116, v80, v116
	v_exp_f32_e32 v58, v58
	v_exp_f32_e32 v59, v59
	v_exp_f32_e32 v60, v60
	v_exp_f32_e32 v61, v61
	v_add_f32_e32 v118, v81, v116
	v_cvt_pk_bf16_f32 v116, v70, v71
	v_cvt_pk_bf16_f32 v117, v72, v73
	s_nop 0
	v_exp_f32_e32 v62, v62
	v_exp_f32_e32 v63, v63
	v_exp_f32_e32 v64, v64
	v_exp_f32_e32 v65, v65
	v_cvt_pk_bf16_f32 v119, v76, v77
	v_add_f32_e32 v70, v118, v50
	v_add_f32_e32 v70, v51, v70
	v_add_f32_e32 v70, v52, v70
	v_add_f32_e32 v122, v53, v70
	v_cvt_pk_bf16_f32 v118, v74, v75
	s_waitcnt lgkmcnt(4)
	v_mfma_f32_32x32x16_bf16 v[98:113], v[246:249], v[142:145], v[98:113]
	ds_read_b128 v[242:245], v184 offset:10240
	ds_read_b128 v[246:249], v184 offset:10752
	s_waitcnt lgkmcnt(5)
	v_mfma_f32_32x32x16_bf16 v[82:97], v[226:229], v[138:141], v[82:97]
	v_add_f32_e32 v120, v122, v54
	v_add_f32_e32 v120, v55, v120
	v_add_f32_e32 v120, v56, v120
	v_add_f32_e32 v122, v57, v120
	v_cvt_pk_bf16_f32 v120, v78, v79
	v_cvt_pk_bf16_f32 v121, v80, v81
	s_nop 0
	v_add_f32_e32 v66, v58, v122
	v_add_f32_e32 v66, v59, v66
	v_add_f32_e32 v66, v60, v66
	v_add_f32_e32 v78, v61, v66
	v_cvt_pk_bf16_f32 v122, v50, v51
	v_cvt_pk_bf16_f32 v123, v52, v53
	s_waitcnt lgkmcnt(4)
	v_mfma_f32_32x32x16_bf16 v[98:113], v[230:233], v[138:141], v[98:113]
	s_waitcnt lgkmcnt(3)
	v_mfma_f32_32x32x16_bf16 v[82:97], v[234:237], v[134:137], v[82:97]
	v_add_f32_e32 v78, v62, v78
	v_add_f32_e32 v78, v63, v78
	v_add_f32_e32 v78, v64, v78
	v_add_f32_e32 v78, v65, v78
	v_cvt_pk_bf16_f32 v124, v54, v55
	v_cvt_pk_bf16_f32 v125, v56, v57
	v_cvt_pk_bf16_f32 v126, v58, v59
	v_cvt_pk_bf16_f32 v127, v60, v61
	s_waitcnt lgkmcnt(2)
	v_mfma_f32_32x32x16_bf16 v[98:113], v[238:241], v[134:137], v[98:113]
	s_waitcnt lgkmcnt(1)
	v_mfma_f32_32x32x16_bf16 v[82:97], v[242:245], v[130:133], v[82:97]
	v_cvt_pk_bf16_f32 v128, v62, v63
	v_cvt_pk_bf16_f32 v129, v64, v65
	s_waitcnt lgkmcnt(0)
; __device__ __forceinline__ float max3f(float a, float b, float c) { float r; asm("v_max3_f32 %0, %1, %2, %3" : "=v"(r) : "v"(a), "v"(b), "v"(c)); return r; }
; __device__ __forceinline__ void cmask(f32x16& p0, f32x16& p1, int jb, int qrel, int hi) {
;     const float NEG = -INFINITY; const int kb = 64 * jb + 4 * hi;
; #pragma unroll
;     for (int r = 0; r < 16; ++r) { const int kv = kb + (r & 3) + 8 * (r >> 2); if (kv > qrel) p0[r] = NEG; if (kv + 32 > qrel) p1[r] = NEG; }
; }
; __device__ __forceinline__ float rowmax(const f32x16& p0, const f32x16& p1) {
;     float a = max3f(p0[0], p0[1], p1[0]), b = max3f(p0[2], p0[3], p1[1]); a = max3f(a, p1[2], p1[3]);
; #pragma unroll
;     for (int r = 4; r < 16; r += 4) { a = max3f(a, p0[r], p0[r + 1]); b = max3f(b, p0[r + 2], p0[r + 3]); a = max3f(a, p1[r], p1[r + 1]); b = max3f(b, p1[r + 2], p1[r + 3]); }
;     const float m = fmaxf(a, b);
;     auto rr = __builtin_amdgcn_permlane32_swap(__float_as_uint(m), __float_as_uint(m), false, false);
;     return fmaxf(__uint_as_float(rr[0]), __uint_as_float(rr[1]));
; }
	v_mfma_f32_32x32x16_bf16 v[98:113], v[246:249], v[130:133], v[98:113]
	v_add_f32_e32 v156, v158, v78
	s_setprio 0
	v_or_b32_e32 v50, 0xa0, v186
	v_or_b32_e32 v51, 0x80, v186
	v_cmp_le_i32_e32 vcc, v50, v182
	v_or_b32_e32 v52, 0x82, v186
	v_or_b32_e32 v53, 0x83, v186
	s_nop 4
	v_cndmask_b32_e32 v50, v206, v98, vcc
	v_cmp_lt_i32_e32 vcc, v51, v182
	v_or_b32_e32 v54, 0x88, v186
	v_or_b32_e32 v55, 0x89, v186
	v_cndmask_b32_e32 v67, v206, v83, vcc
	v_cmp_le_i32_e32 vcc, v51, v182
	v_or_b32_e32 v51, 0xa1, v186
	v_or_b32_e32 v56, 0x8a, v186
	v_cndmask_b32_e32 v66, v206, v82, vcc
	v_cmp_le_i32_e32 vcc, v51, v182
	v_or_b32_e32 v57, 0x8b, v186
	v_or_b32_e32 v58, 0x90, v186
	v_cndmask_b32_e32 v51, v206, v99, vcc
	v_cmp_le_i32_e32 vcc, v52, v182
	v_or_b32_e32 v52, 0xa2, v186
	v_or_b32_e32 v59, 0x91, v186
	v_cndmask_b32_e32 v68, v206, v84, vcc
	v_cmp_le_i32_e32 vcc, v52, v182
	v_or_b32_e32 v60, 0x92, v186
	v_or_b32_e32 v61, 0x93, v186
	v_cndmask_b32_e32 v52, v206, v100, vcc
	v_cmp_le_i32_e32 vcc, v53, v182
	v_or_b32_e32 v53, 0xa3, v186
	v_or_b32_e32 v62, 0x98, v186
	v_cndmask_b32_e32 v69, v206, v85, vcc
	v_cmp_le_i32_e32 vcc, v53, v182
	v_or_b32_e32 v63, 0x99, v186
	v_max3_f32 v82, v66, v67, v50
	v_max3_f32 v83, v68, v69, v51
	v_or_b32_e32 v64, 0x9a, v186
	v_cndmask_b32_e32 v53, v206, v101, vcc
	v_cmp_le_i32_e32 vcc, v54, v182
	v_or_b32_e32 v54, 0xa8, v186
	v_max3_f32 v82, v82, v52, v53
	v_or_b32_e32 v65, 0x9b, v186
	v_cndmask_b32_e32 v70, v206, v86, vcc
	v_cmp_le_i32_e32 vcc, v54, v182
	s_nop 1
	v_cndmask_b32_e32 v54, v206, v102, vcc
	v_cmp_le_i32_e32 vcc, v55, v182
	v_or_b32_e32 v55, 0xa9, v186
	s_nop 0
	v_cndmask_b32_e32 v71, v206, v87, vcc
	v_cmp_le_i32_e32 vcc, v55, v182
	v_max3_f32 v82, v82, v70, v71
	s_nop 1
	v_cndmask_b32_e32 v55, v206, v103, vcc
	v_cmp_le_i32_e32 vcc, v56, v182
	v_or_b32_e32 v56, 0xaa, v186
	v_max3_f32 v82, v82, v54, v55
	s_nop 0
	v_cndmask_b32_e32 v72, v206, v88, vcc
	v_cmp_le_i32_e32 vcc, v56, v182
	s_nop 1
	v_cndmask_b32_e32 v56, v206, v104, vcc
	v_cmp_le_i32_e32 vcc, v57, v182
	v_or_b32_e32 v57, 0xab, v186
	s_nop 0
	v_cndmask_b32_e32 v73, v206, v89, vcc
	v_cmp_le_i32_e32 vcc, v57, v182
	v_max3_f32 v83, v83, v72, v73
	s_nop 1
	v_cndmask_b32_e32 v57, v206, v105, vcc
	v_cmp_le_i32_e32 vcc, v58, v182
	v_or_b32_e32 v58, 0xb0, v186
	v_max3_f32 v83, v83, v56, v57
	s_nop 0
	v_cndmask_b32_e32 v74, v206, v90, vcc
	v_cmp_le_i32_e32 vcc, v58, v182
	s_nop 1
	v_cndmask_b32_e32 v58, v206, v106, vcc
	v_cmp_le_i32_e32 vcc, v59, v182
	v_or_b32_e32 v59, 0xb1, v186
	s_nop 0
	v_cndmask_b32_e32 v75, v206, v91, vcc
	v_cmp_le_i32_e32 vcc, v59, v182
	v_max3_f32 v82, v82, v74, v75
	s_nop 1
	v_cndmask_b32_e32 v59, v206, v107, vcc
	v_cmp_le_i32_e32 vcc, v60, v182
	v_or_b32_e32 v60, 0xb2, v186
	v_max3_f32 v82, v82, v58, v59
	s_nop 0
	v_cndmask_b32_e32 v76, v206, v92, vcc
	v_cmp_le_i32_e32 vcc, v60, v182
	s_nop 1
	v_cndmask_b32_e32 v60, v206, v108, vcc
	v_cmp_le_i32_e32 vcc, v61, v182
	v_or_b32_e32 v61, 0xb3, v186
	s_nop 0
	v_cndmask_b32_e32 v77, v206, v93, vcc
	v_cmp_le_i32_e32 vcc, v61, v182
	v_max3_f32 v83, v83, v76, v77
	s_nop 1
	v_cndmask_b32_e32 v61, v206, v109, vcc
	v_cmp_le_i32_e32 vcc, v62, v182
	v_or_b32_e32 v62, 0xb8, v186
	v_max3_f32 v83, v83, v60, v61
	s_nop 0
	v_cndmask_b32_e32 v78, v206, v94, vcc
	v_cmp_le_i32_e32 vcc, v62, v182
	s_nop 1
	v_cndmask_b32_e32 v62, v206, v110, vcc
	v_cmp_le_i32_e32 vcc, v63, v182
	v_or_b32_e32 v63, 0xb9, v186
	s_nop 0
	v_cndmask_b32_e32 v79, v206, v95, vcc
	v_cmp_le_i32_e32 vcc, v63, v182
	v_max3_f32 v82, v82, v78, v79
	s_nop 1
	v_cndmask_b32_e32 v63, v206, v111, vcc
	v_cmp_le_i32_e32 vcc, v64, v182
	v_or_b32_e32 v64, 0xba, v186
	v_max3_f32 v82, v82, v62, v63
	s_nop 0
	v_cndmask_b32_e32 v80, v206, v96, vcc
	v_cmp_le_i32_e32 vcc, v64, v182
	v_max_f32_e32 v82, v82, v82
	s_nop 0
	v_cndmask_b32_e32 v64, v206, v112, vcc
	v_cmp_le_i32_e32 vcc, v65, v182
	v_or_b32_e32 v65, 0xbb, v186
	s_nop 0
	v_cndmask_b32_e32 v81, v206, v97, vcc
	v_cmp_le_i32_e32 vcc, v65, v182
	v_max3_f32 v83, v83, v80, v81
	s_nop 1
	v_cndmask_b32_e32 v65, v206, v113, vcc
	v_max3_f32 v83, v83, v64, v65
	s_nop 0
	v_max_f32_e32 v83, v83, v83
	v_max_f32_e32 v82, v82, v83
	v_mov_b32_e32 v83, v82
	s_nop 1
	v_permlane32_swap_b32_e32 v82, v83
	v_max_f32_e32 v83, v83, v83
	v_max_f32_e32 v82, v82, v82
	v_max_f32_e32 v82, v82, v83
	v_cmp_lt_f32_e32 vcc, s54, v82
	s_cmp_lg_u64 vcc, 0
	s_cselect_b64 s[0:1], -1, 0
	s_cbranch_vccnz .LBB0_1214

.LBB0_1139:
	s_setprio 1
	ds_read_b128 v[226:229], v183
	ds_read_b128 v[230:233], v183 offset:512
	ds_read_b128 v[234:237], v183 offset:2048
	ds_read_b128 v[238:241], v183 offset:2560
	ds_read_b128 v[242:245], v183 offset:4096
	ds_read_b128 v[246:249], v183 offset:4608
	v_exp_f32_e32 v66, v66
	v_exp_f32_e32 v67, v67
	v_exp_f32_e32 v68, v68
	v_exp_f32_e32 v69, v69
	s_nop 0
	v_exp_f32_e32 v70, v70
	v_exp_f32_e32 v71, v71
	v_exp_f32_e32 v72, v72
	v_exp_f32_e32 v73, v73
	v_exp_f32_e32 v74, v74
	v_exp_f32_e32 v75, v75
	v_exp_f32_e32 v76, v76
	v_exp_f32_e32 v77, v77
	s_waitcnt lgkmcnt(5)
	v_mfma_f32_32x32x16_bf16 v[82:97], v[226:229], v[150:153], v[34:49]
	s_waitcnt lgkmcnt(4)
	v_mfma_f32_32x32x16_bf16 v[34:49], v[230:233], v[150:153], v[34:49]
	ds_read_b128 v[226:229], v183 offset:6144
	ds_read_b128 v[230:233], v183 offset:6656
	v_exp_f32_e32 v78, v78
	v_exp_f32_e32 v79, v79
	v_exp_f32_e32 v80, v80
	v_exp_f32_e32 v81, v81
	s_nop 0
	v_add_f32_e32 v98, 0, v66
	v_add_f32_e32 v98, v67, v98
	v_add_f32_e32 v98, v68, v98
	v_add_f32_e32 v114, v69, v98
	s_waitcnt lgkmcnt(5)
	v_mfma_f32_32x32x16_bf16 v[82:97], v[234:237], v[146:149], v[82:97]
	v_add_f32_e32 v106, v114, v70
	v_add_f32_e32 v106, v71, v106
	v_add_f32_e32 v106, v72, v106
	v_exp_f32_e32 v50, v50
	v_exp_f32_e32 v51, v51
	v_exp_f32_e32 v52, v52
	v_exp_f32_e32 v53, v53
	v_add_f32_e32 v106, v73, v106
	s_waitcnt lgkmcnt(4)
	v_mfma_f32_32x32x16_bf16 v[34:49], v[238:241], v[146:149], v[34:49]
	ds_read_b128 v[234:237], v183 offset:8192
	ds_read_b128 v[238:241], v183 offset:8704
	v_add_f32_e32 v106, v74, v106
	v_add_f32_e32 v106, v75, v106
	v_add_f32_e32 v106, v76, v106
	v_exp_f32_e32 v54, v54
	v_exp_f32_e32 v55, v55
	v_exp_f32_e32 v56, v56
	v_exp_f32_e32 v57, v57
	v_add_f32_e32 v110, v77, v106
	v_cvt_pk_bf16_f32 v114, v66, v67
	v_cvt_pk_bf16_f32 v115, v68, v69
	s_waitcnt lgkmcnt(5)
	v_mfma_f32_32x32x16_bf16 v[82:97], v[242:245], v[142:145], v[82:97]
	v_add_f32_e32 v98, v78, v110
	v_add_f32_e32 v98, v79, v98
	v_add_f32_e32 v98, v80, v98
	v_exp_f32_e32 v58, v58
	v_exp_f32_e32 v59, v59
	v_exp_f32_e32 v60, v60
	v_exp_f32_e32 v61, v61
	v_add_f32_e32 v98, v81, v98
	v_cvt_pk_bf16_f32 v116, v70, v71
	v_cvt_pk_bf16_f32 v117, v72, v73
	s_waitcnt lgkmcnt(4)
	v_mfma_f32_32x32x16_bf16 v[34:49], v[246:249], v[142:145], v[34:49]
	ds_read_b128 v[242:245], v183 offset:10240
	ds_read_b128 v[246:249], v183 offset:10752
	v_exp_f32_e32 v62, v62
	v_exp_f32_e32 v63, v63
	v_exp_f32_e32 v64, v64
	v_exp_f32_e32 v65, v65
	v_cvt_pk_bf16_f32 v118, v74, v75
	v_add_f32_e32 v70, v98, v50
	v_add_f32_e32 v70, v51, v70
	v_add_f32_e32 v70, v52, v70
	v_add_f32_e32 v98, v53, v70
	v_cvt_pk_bf16_f32 v119, v76, v77
	v_add_f32_e32 v98, v98, v54
	v_add_f32_e32 v98, v55, v98
	v_add_f32_e32 v98, v56, v98
	v_add_f32_e32 v98, v57, v98
	v_cvt_pk_bf16_f32 v120, v78, v79
	v_cvt_pk_bf16_f32 v121, v80, v81
	s_waitcnt lgkmcnt(5)
	v_mfma_f32_32x32x16_bf16 v[82:97], v[226:229], v[138:141], v[82:97]
	s_waitcnt lgkmcnt(4)
	v_mfma_f32_32x32x16_bf16 v[34:49], v[230:233], v[138:141], v[34:49]
	v_add_f32_e32 v66, v58, v98
	v_add_f32_e32 v66, v59, v66
	v_add_f32_e32 v66, v60, v66
	v_add_f32_e32 v78, v61, v66
	v_cvt_pk_bf16_f32 v122, v50, v51
	v_cvt_pk_bf16_f32 v123, v52, v53
	v_add_f32_e32 v78, v62, v78
	v_add_f32_e32 v78, v63, v78
	v_add_f32_e32 v78, v64, v78
	v_add_f32_e32 v78, v65, v78
	v_cvt_pk_bf16_f32 v124, v54, v55
	v_cvt_pk_bf16_f32 v125, v56, v57
	s_waitcnt lgkmcnt(3)
	v_mfma_f32_32x32x16_bf16 v[82:97], v[234:237], v[134:137], v[82:97]
	s_waitcnt lgkmcnt(2)
	v_mfma_f32_32x32x16_bf16 v[34:49], v[238:241], v[134:137], v[34:49]
	v_cvt_pk_bf16_f32 v126, v58, v59
	v_cvt_pk_bf16_f32 v127, v60, v61
	s_nop 0
	v_cvt_pk_bf16_f32 v128, v62, v63
	v_cvt_pk_bf16_f32 v129, v64, v65
	s_waitcnt lgkmcnt(1)
	v_mfma_f32_32x32x16_bf16 v[82:97], v[242:245], v[130:133], v[82:97]
	s_waitcnt lgkmcnt(0)
; __device__ __forceinline__ float max3f(float a, float b, float c) { float r; asm("v_max3_f32 %0, %1, %2, %3" : "=v"(r) : "v"(a), "v"(b), "v"(c)); return r; }
; __device__ __forceinline__ void cmask(f32x16& p0, f32x16& p1, int jb, int qrel, int hi) {
;     const float NEG = -INFINITY; const int kb = 64 * jb + 4 * hi;
; #pragma unroll
;     for (int r = 0; r < 16; ++r) { const int kv = kb + (r & 3) + 8 * (r >> 2); if (kv > qrel) p0[r] = NEG; if (kv + 32 > qrel) p1[r] = NEG; }
; }
; __device__ __forceinline__ float rowmax(const f32x16& p0, const f32x16& p1) {
;     float a = max3f(p0[0], p0[1], p1[0]), b = max3f(p0[2], p0[3], p1[1]); a = max3f(a, p1[2], p1[3]);
; #pragma unroll
;     for (int r = 4; r < 16; r += 4) { a = max3f(a, p0[r], p0[r + 1]); b = max3f(b, p0[r + 2], p0[r + 3]); a = max3f(a, p1[r], p1[r + 1]); b = max3f(b, p1[r + 2], p1[r + 3]); }
;     const float m = fmaxf(a, b);
;     auto rr = __builtin_amdgcn_permlane32_swap(__float_as_uint(m), __float_as_uint(m), false, false);
;     return fmaxf(__uint_as_float(rr[0]), __uint_as_float(rr[1]));
; }
	v_mfma_f32_32x32x16_bf16 v[34:49], v[246:249], v[130:133], v[34:49]
	v_add_f32_e32 v98, v156, v78
	s_setprio 0
	v_or_b32_e32 v51, 0xe0, v186
	v_or_b32_e32 v50, 0xc0, v186
	v_cmp_le_i32_e32 vcc, v51, v182
	v_or_b32_e32 v52, 0xe1, v186
	v_or_b32_e32 v53, 0xe2, v186
	s_nop 4
	v_cndmask_b32_e32 v34, v206, v34, vcc
	v_cmp_lt_i32_e32 vcc, v50, v182
	v_or_b32_e32 v54, 0xe3, v186
	v_or_b32_e32 v55, 0xe8, v186
	v_cndmask_b32_e32 v51, v206, v83, vcc
	v_cmp_le_i32_e32 vcc, v50, v182
	v_or_b32_e32 v56, 0xe9, v186
	v_or_b32_e32 v57, 0xea, v186
	v_cndmask_b32_e32 v50, v206, v82, vcc
	v_cmp_le_i32_e32 vcc, v52, v182
	v_or_b32_e32 v52, 0xc2, v186
	v_or_b32_e32 v58, 0xeb, v186
	v_cndmask_b32_e32 v35, v206, v35, vcc
	v_cmp_le_i32_e32 vcc, v52, v182
	v_or_b32_e32 v59, 0xf0, v186
	v_or_b32_e32 v60, 0xf1, v186
	v_cndmask_b32_e32 v52, v206, v84, vcc
	v_cmp_le_i32_e32 vcc, v53, v182
	v_or_b32_e32 v53, 0xc3, v186
	v_or_b32_e32 v61, 0xf2, v186
	v_cndmask_b32_e32 v36, v206, v36, vcc
	v_cmp_le_i32_e32 vcc, v53, v182
	v_or_b32_e32 v62, 0xf3, v186
	v_or_b32_e32 v63, 0xf8, v186
	v_cndmask_b32_e32 v53, v206, v85, vcc
	v_cmp_le_i32_e32 vcc, v54, v182
	v_or_b32_e32 v54, 0xc8, v186
	v_or_b32_e32 v64, 0xf9, v186
	v_cndmask_b32_e32 v37, v206, v37, vcc
	v_cmp_le_i32_e32 vcc, v54, v182
	v_or_b32_e32 v65, 0xfa, v186
	v_or_b32_e32 v66, 0xfb, v186
	v_cndmask_b32_e32 v54, v206, v86, vcc
	v_cmp_le_i32_e32 vcc, v55, v182
	v_or_b32_e32 v55, 0xc9, v186
	v_max3_f32 v67, v52, v53, v35
	s_nop 0
	v_cndmask_b32_e32 v38, v206, v38, vcc
	v_cmp_le_i32_e32 vcc, v55, v182
	s_nop 1
	v_cndmask_b32_e32 v55, v206, v87, vcc
	v_cmp_le_i32_e32 vcc, v56, v182
	v_or_b32_e32 v56, 0xca, v186
	s_nop 0
	v_cndmask_b32_e32 v39, v206, v39, vcc
	v_cmp_le_i32_e32 vcc, v56, v182
	s_nop 1
	v_cndmask_b32_e32 v56, v206, v88, vcc
	v_cmp_le_i32_e32 vcc, v57, v182
	v_or_b32_e32 v57, 0xcb, v186
	s_nop 0
	v_cndmask_b32_e32 v40, v206, v40, vcc
	v_cmp_le_i32_e32 vcc, v57, v182
	s_nop 1
	v_cndmask_b32_e32 v57, v206, v89, vcc
	v_cmp_le_i32_e32 vcc, v58, v182
	v_or_b32_e32 v58, 0xd0, v186
	v_max3_f32 v67, v67, v56, v57
	s_nop 0
	v_cndmask_b32_e32 v41, v206, v41, vcc
	v_cmp_le_i32_e32 vcc, v58, v182
	v_max3_f32 v67, v67, v40, v41
	s_nop 1
	v_cndmask_b32_e32 v58, v206, v90, vcc
	v_cmp_le_i32_e32 vcc, v59, v182
	v_or_b32_e32 v59, 0xd1, v186
	s_nop 0
	v_cndmask_b32_e32 v42, v206, v42, vcc
	v_cmp_le_i32_e32 vcc, v59, v182
	s_nop 1
	v_cndmask_b32_e32 v59, v206, v91, vcc
	v_cmp_le_i32_e32 vcc, v60, v182
	v_or_b32_e32 v60, 0xd2, v186
	s_nop 0
	v_cndmask_b32_e32 v43, v206, v43, vcc
	v_cmp_le_i32_e32 vcc, v60, v182
	s_nop 1
	v_cndmask_b32_e32 v60, v206, v92, vcc
	v_cmp_le_i32_e32 vcc, v61, v182
	v_or_b32_e32 v61, 0xd3, v186
	s_nop 0
	v_cndmask_b32_e32 v44, v206, v44, vcc
	v_cmp_le_i32_e32 vcc, v61, v182
	s_nop 1
	v_cndmask_b32_e32 v61, v206, v93, vcc
	v_cmp_le_i32_e32 vcc, v62, v182
	v_or_b32_e32 v62, 0xd8, v186
	v_max3_f32 v67, v67, v60, v61
	s_nop 0
	v_cndmask_b32_e32 v45, v206, v45, vcc
	v_cmp_le_i32_e32 vcc, v62, v182
	v_max3_f32 v67, v67, v44, v45
	s_nop 1
	v_cndmask_b32_e32 v62, v206, v94, vcc
	v_cmp_le_i32_e32 vcc, v63, v182
	v_or_b32_e32 v63, 0xd9, v186
	s_nop 0
	v_cndmask_b32_e32 v46, v206, v46, vcc
	v_cmp_le_i32_e32 vcc, v63, v182
	s_nop 1
	v_cndmask_b32_e32 v63, v206, v95, vcc
	v_cmp_le_i32_e32 vcc, v64, v182
	v_or_b32_e32 v64, 0xda, v186
	s_nop 0
	v_cndmask_b32_e32 v47, v206, v47, vcc
	v_cmp_le_i32_e32 vcc, v64, v182
	s_nop 1
	v_cndmask_b32_e32 v64, v206, v96, vcc
	v_cmp_le_i32_e32 vcc, v65, v182
	v_or_b32_e32 v65, 0xdb, v186
	s_nop 0
	v_cndmask_b32_e32 v48, v206, v48, vcc
	v_cmp_le_i32_e32 vcc, v65, v182
	s_nop 1
	v_cndmask_b32_e32 v65, v206, v97, vcc
	v_cmp_le_i32_e32 vcc, v66, v182
	v_max3_f32 v66, v50, v51, v34
	v_max3_f32 v67, v67, v64, v65
	s_nop 0
	v_max3_f32 v66, v66, v36, v37
	s_nop 0
	v_max3_f32 v66, v66, v54, v55
	v_cndmask_b32_e32 v49, v206, v49, vcc
	v_max3_f32 v66, v66, v38, v39
	v_max3_f32 v67, v67, v48, v49
	s_nop 0
	v_max3_f32 v66, v66, v58, v59
	v_max_f32_e32 v67, v67, v67
	v_max3_f32 v66, v66, v42, v43
	s_nop 0
	v_max3_f32 v66, v66, v62, v63
	s_nop 0
	v_max3_f32 v66, v66, v46, v47
	s_nop 0
	v_max_f32_e32 v66, v66, v66
	v_max_f32_e32 v66, v66, v67
	v_mov_b32_e32 v67, v66
	s_nop 1
	v_permlane32_swap_b32_e32 v66, v67
	v_max_f32_e32 v67, v67, v67
	v_max_f32_e32 v66, v66, v66
	v_max_f32_e32 v66, v66, v67
	v_cmp_lt_f32_e32 vcc, s54, v66
	s_cmp_lg_u64 vcc, 0
	s_cselect_b64 s[0:1], -1, 0
	s_cbranch_vccnz .LBB0_1217

; #define MLA_WAIT_BAR(N) asm volatile("s_waitcnt vmcnt(" #N ") lgkmcnt(0)\n\ts_barrier" ::: "memory")
; #define MLA_PIN(x) asm volatile("" : "+v"(x))
; #define MLA_LDK(kp, d0, h) (*(const __attribute__((address_space(3))) bf16x8*)((kp) + (d0) * 2048 + (h) * 512))
; #define MLA_MF(C, K, Q) C = __builtin_amdgcn_mfma_f32_32x32x16_bf16(K, Q, C, 0, 0, 0)
; template <int THRL, bool LATE> __device__ __forceinline__ void unit_stag(int b, int h, int qb, const unsigned short* Q, const unsigned short* KV, const unsigned short* KPE, unsigned short* O, char* shm, const int wave_) {
;     ...
;     glds16(ksrc + (long)2 * KVBLK * KVP, (unsigned)__builtin_amdgcn_readfirstlane(kdst + 2 * KSLOT)); if (lane < 32) glds16(psrc + (long)2 * KVBLK * PEP, (unsigned)__builtin_amdgcn_readfirstlane(pdst + 2 * KSLOT)); glds16(vsrc + (long)KVBLK * KVP, (unsigned)__builtin_amdgcn_readfirstlane(vdst + VSLOT));
;     float mhat = 0.f, l_reg = 0.f; f32x16 o[2]; o[0] = f32x16{}; o[1] = f32x16{}; f32x16 negm = f32x16{}; MLA_PIN(negm);
;     const int qrel = wid * QBLK + r32; bool resc = false;
;     f32x16 pA0, pA1, pB0, pB1; u32x4 pw0, pw1, pw2, pw3;
;     int s0 = 0, s1 = 1, s2 = 2;
;     MLA_WAIT_BAR(6);
;     { const lds_cptr kp = kp0;
;       pA0 = f32x16{}; pA1 = f32x16{};
; #pragma unroll
;       for (int d0 = 0; d0 < 6; ++d0) { const bf16x8 k0 = MLA_LDK(kp, d0, 0), k1 = MLA_LDK(kp, d0, 1); MLA_MF(pA0, k0, qr[d0]); MLA_MF(pA1, k1, qr[d0]); } }
;     { const float rm_ = rowmax(pA0, pA1); mhat = rm_;
; #pragma unroll
;       for (int r = 0; r < 16; ++r) { pA0[r] -= rm_; pA1[r] -= rm_; negm[r] = -mhat; }
;       MLA_PIN(negm); }
.LBB0_1152:
	s_or_b64 exec, exec, s[0:1]
	s_cmp_lg_u32 0, -1
	v_lshlrev_b32_e32 v0, 10, v210
	v_lshlrev_b32_e32 v2, 4, v209
	s_cselect_b32 s0, 0, 0
	v_add3_u32 v213, 0, v0, v2
	v_lshl_add_u64 v[2:3], v[200:201], 0, s[12:13]
	s_add_i32 s0, s0, s42
	s_add_i32 s0, s0, 0xb000
	s_mov_b32 s1, m0
	s_mov_b32 m0, s0
	s_nop 0
	global_load_lds_dwordx4 v[2:3], off
	s_mov_b32 m0, s1
	v_mov_b32_e32 v2, v1
	v_mov_b32_e32 v3, v1
	v_mov_b32_e32 v4, v1
	v_mov_b32_e32 v5, v1
	v_mov_b32_e32 v6, v1
	v_mov_b32_e32 v7, v1
	v_mov_b32_e32 v8, v1
	v_mov_b32_e32 v9, v1
	v_mov_b32_e32 v10, v1
	v_mov_b32_e32 v11, v1
	v_mov_b32_e32 v12, v1
	v_mov_b32_e32 v13, v1
	v_mov_b32_e32 v14, v1
	v_mov_b32_e32 v15, v1
	v_mov_b32_e32 v0, v1
	v_mov_b64_e32 v[16:17], v[14:15]
	v_mov_b64_e32 v[14:15], v[12:13]
	v_mov_b64_e32 v[12:13], v[10:11]
	v_mov_b64_e32 v[10:11], v[8:9]
	v_mov_b64_e32 v[8:9], v[6:7]
	v_mov_b64_e32 v[6:7], v[4:5]
	v_mov_b64_e32 v[4:5], v[2:3]
	v_mov_b64_e32 v[2:3], v[0:1]
	s_waitcnt vmcnt(6) lgkmcnt(0)
	s_barrier
	ds_read_b128 v[2:5], v213
	ds_read_b128 v[6:9], v213 offset:512
	s_waitcnt vmcnt(5) lgkmcnt(1)
	v_mfma_f32_32x32x16_bf16 v[18:33], v[2:5], v[196:199], 0
	ds_read_b128 v[36:39], v213 offset:2048
	ds_read_b128 v[40:43], v213 offset:2560
	s_waitcnt lgkmcnt(2)
	v_mfma_f32_32x32x16_bf16 v[2:17], v[6:9], v[196:199], 0
	s_waitcnt vmcnt(4) lgkmcnt(1)
	v_mfma_f32_32x32x16_bf16 v[18:33], v[36:39], v[192:195], v[18:33]
	s_waitcnt lgkmcnt(0)
	v_mfma_f32_32x32x16_bf16 v[2:17], v[40:43], v[192:195], v[2:17]
	ds_read_b128 v[36:39], v213 offset:4096
	ds_read_b128 v[40:43], v213 offset:4608
	s_waitcnt vmcnt(3) lgkmcnt(1)
	v_mfma_f32_32x32x16_bf16 v[18:33], v[36:39], v[188:191], v[18:33]
	s_waitcnt lgkmcnt(0)
	v_mfma_f32_32x32x16_bf16 v[2:17], v[40:43], v[188:191], v[2:17]
	ds_read_b128 v[36:39], v213 offset:6144
	ds_read_b128 v[40:43], v213 offset:6656
	s_waitcnt vmcnt(2) lgkmcnt(1)
	v_mfma_f32_32x32x16_bf16 v[18:33], v[36:39], v[184:187], v[18:33]
	s_waitcnt lgkmcnt(0)
	v_mfma_f32_32x32x16_bf16 v[2:17], v[40:43], v[184:187], v[2:17]
	ds_read_b128 v[36:39], v213 offset:8192
	ds_read_b128 v[40:43], v213 offset:8704
	s_waitcnt vmcnt(1) lgkmcnt(1)
	v_mfma_f32_32x32x16_bf16 v[18:33], v[36:39], v[180:183], v[18:33]
	s_waitcnt lgkmcnt(0)
	v_mfma_f32_32x32x16_bf16 v[2:17], v[40:43], v[180:183], v[2:17]
	ds_read_b128 v[36:39], v213 offset:10240
	ds_read_b128 v[40:43], v213 offset:10752
	s_waitcnt vmcnt(0) lgkmcnt(1)
	v_mfma_f32_32x32x16_bf16 v[18:33], v[36:39], v[176:179], v[18:33]
	s_waitcnt lgkmcnt(0)
	v_mfma_f32_32x32x16_bf16 v[2:17], v[40:43], v[176:179], v[2:17]
	v_max3_f32 v0, v18, v19, v2
	v_max3_f32 v36, v20, v21, v3
	s_nop 0
	v_max3_f32 v0, v0, v4, v5
	v_max3_f32 v36, v36, v24, v25
	s_nop 0
	v_max3_f32 v0, v0, v22, v23
	v_max3_f32 v36, v36, v8, v9
	s_nop 0
	v_max3_f32 v0, v0, v6, v7
	v_max3_f32 v36, v36, v28, v29
	s_nop 0
	v_max3_f32 v0, v0, v26, v27
	v_max3_f32 v36, v36, v12, v13
	s_nop 0
	v_max3_f32 v0, v0, v10, v11
	v_max3_f32 v36, v36, v32, v33
	s_nop 0
	v_max3_f32 v0, v0, v30, v31
	v_max3_f32 v36, v36, v16, v17
	s_nop 0
	v_max3_f32 v0, v0, v14, v15
	v_max_f32_e32 v36, v36, v36
	v_max_f32_e32 v0, v0, v0
	v_max_f32_e32 v0, v0, v36
	v_mov_b32_e32 v36, v0
	s_nop 1
	v_permlane32_swap_b32_e32 v0, v36
	v_max_f32_e32 v36, v36, v36
	v_max_f32_e32 v0, v0, v0
	v_max_f32_e32 v0, v0, v36
	v_xor_b32_e32 v82, 0x80000000, v0
	v_mov_b32_e32 v83, v82
	v_mov_b32_e32 v84, v82
	v_mov_b32_e32 v85, v82
	v_mov_b32_e32 v86, v82
	v_mov_b32_e32 v87, v82
	v_mov_b32_e32 v88, v82
	v_mov_b32_e32 v89, v82
	v_mov_b32_e32 v90, v82
	v_mov_b32_e32 v91, v82
	v_mov_b32_e32 v92, v82
	v_mov_b32_e32 v93, v82
	v_mov_b32_e32 v94, v82
	v_mov_b32_e32 v95, v82
	v_mov_b32_e32 v96, v82
	v_mov_b32_e32 v97, v82
	s_waitcnt vmcnt(3) lgkmcnt(0)
	s_barrier
; #define MLA_PIN(x) asm volatile("" : "+v"(x))
; template <int THRL, bool LATE> __device__ __forceinline__ void unit_stag(int b, int h, int qb, const unsigned short* Q, const unsigned short* KV, const unsigned short* KPE, unsigned short* O, char* shm, const int wave_) {
;     ...
;     { const float rm_ = rowmax(pA0, pA1); mhat = rm_;
; #pragma unroll
;       for (int r = 0; r < 16; ++r) { pA0[r] -= rm_; pA1[r] -= rm_; negm[r] = -mhat; }
;       MLA_PIN(negm); }
;     int t = 0;
;     MLA_STEPS(pB0, pB1, pA0, pA1, t, -1, 3, true, true, false); ++t;
	v_sub_f32_e32 v48, v2, v0
	v_sub_f32_e32 v2, v19, v0
	v_sub_f32_e32 v18, v18, v0
	v_sub_f32_e32 v49, v3, v0
	v_sub_f32_e32 v3, v20, v0
	v_sub_f32_e32 v50, v4, v0
	v_sub_f32_e32 v4, v21, v0
	v_sub_f32_e32 v51, v5, v0
	v_pk_add_f32 v[22:23], v[22:23], v[0:1] op_sel_hi:[1,0] neg_lo:[0,1] neg_hi:[0,1]
	v_pk_add_f32 v[6:7], v[6:7], v[0:1] op_sel_hi:[1,0] neg_lo:[0,1] neg_hi:[0,1]
	v_pk_add_f32 v[24:25], v[24:25], v[0:1] op_sel_hi:[1,0] neg_lo:[0,1] neg_hi:[0,1]
	v_pk_add_f32 v[8:9], v[8:9], v[0:1] op_sel_hi:[1,0] neg_lo:[0,1] neg_hi:[0,1]
	v_pk_add_f32 v[26:27], v[26:27], v[0:1] op_sel_hi:[1,0] neg_lo:[0,1] neg_hi:[0,1]
	v_pk_add_f32 v[10:11], v[10:11], v[0:1] op_sel_hi:[1,0] neg_lo:[0,1] neg_hi:[0,1]
	v_pk_add_f32 v[28:29], v[28:29], v[0:1] op_sel_hi:[1,0] neg_lo:[0,1] neg_hi:[0,1]
	v_pk_add_f32 v[12:13], v[12:13], v[0:1] op_sel_hi:[1,0] neg_lo:[0,1] neg_hi:[0,1]
	v_pk_add_f32 v[30:31], v[30:31], v[0:1] op_sel_hi:[1,0] neg_lo:[0,1] neg_hi:[0,1]
	v_pk_add_f32 v[14:15], v[14:15], v[0:1] op_sel_hi:[1,0] neg_lo:[0,1] neg_hi:[0,1]
	v_pk_add_f32 v[32:33], v[32:33], v[0:1] op_sel_hi:[1,0] neg_lo:[0,1] neg_hi:[0,1]
	v_pk_add_f32 v[16:17], v[16:17], v[0:1] op_sel_hi:[1,0] neg_lo:[0,1] neg_hi:[0,1]
	s_setprio 1
	ds_read_b128 v[226:229], v213 offset:12288
	ds_read_b128 v[230:233], v213 offset:12800
	ds_read_b128 v[234:237], v213 offset:14336
	ds_read_b128 v[238:241], v213 offset:14848
	ds_read_b128 v[242:245], v213 offset:16384
	ds_read_b128 v[246:249], v213 offset:16896
	v_exp_f32_e32 v19, v2
	v_exp_f32_e32 v20, v3
	v_exp_f32_e32 v21, v4
	v_exp_f32_e32 v18, v18
	s_nop 0
	v_exp_f32_e32 v22, v22
	v_exp_f32_e32 v23, v23
	v_exp_f32_e32 v24, v24
	v_exp_f32_e32 v25, v25
	s_waitcnt lgkmcnt(5)
	v_mfma_f32_32x32x16_bf16 v[98:113], v[226:229], v[196:199], v[82:97]
	v_exp_f32_e32 v26, v26
	v_exp_f32_e32 v27, v27
	v_exp_f32_e32 v28, v28
	v_exp_f32_e32 v29, v29
	s_waitcnt lgkmcnt(4)
	v_mfma_f32_32x32x16_bf16 v[114:129], v[230:233], v[196:199], v[82:97]
	ds_read_b128 v[226:229], v213 offset:18432
	ds_read_b128 v[230:233], v213 offset:18944
	v_exp_f32_e32 v30, v30
	v_exp_f32_e32 v31, v31
	v_exp_f32_e32 v32, v32
	v_exp_f32_e32 v33, v33
	s_nop 0
	v_add_f32_e32 v2, 0, v18
	v_add_f32_e32 v2, v19, v2
	v_add_f32_e32 v2, v20, v2
	v_add_f32_e32 v52, v21, v2
	s_waitcnt lgkmcnt(5)
	v_mfma_f32_32x32x16_bf16 v[98:113], v[234:237], v[192:195], v[98:113]
	v_exp_f32_e32 v2, v48
	v_exp_f32_e32 v3, v49
	v_exp_f32_e32 v4, v50
	v_exp_f32_e32 v5, v51
	v_add_f32_e32 v40, v52, v22
	v_add_f32_e32 v40, v23, v40
	v_add_f32_e32 v40, v24, v40
	v_add_f32_e32 v40, v25, v40
	s_waitcnt lgkmcnt(4)
	v_mfma_f32_32x32x16_bf16 v[114:129], v[238:241], v[192:195], v[114:129]
	ds_read_b128 v[234:237], v213 offset:20480
	ds_read_b128 v[238:241], v213 offset:20992
	v_add_f32_e32 v40, v26, v40
	v_add_f32_e32 v40, v27, v40
	v_add_f32_e32 v40, v28, v40
	v_exp_f32_e32 v6, v6
	v_exp_f32_e32 v7, v7
	v_exp_f32_e32 v8, v8
	v_exp_f32_e32 v9, v9
	v_add_f32_e32 v44, v29, v40
	v_cvt_pk_bf16_f32 v160, v18, v19
	v_cvt_pk_bf16_f32 v161, v20, v21
	s_waitcnt lgkmcnt(5)
	v_mfma_f32_32x32x16_bf16 v[98:113], v[242:245], v[188:191], v[98:113]
	v_add_f32_e32 v36, v30, v44
	v_add_f32_e32 v36, v31, v36
	v_add_f32_e32 v36, v32, v36
	v_exp_f32_e32 v10, v10
	v_exp_f32_e32 v11, v11
	v_exp_f32_e32 v12, v12
	v_exp_f32_e32 v13, v13
	v_add_f32_e32 v36, v33, v36
	v_cvt_pk_bf16_f32 v162, v22, v23
	v_cvt_pk_bf16_f32 v163, v24, v25
	s_waitcnt lgkmcnt(4)
	v_mfma_f32_32x32x16_bf16 v[114:129], v[246:249], v[188:191], v[114:129]
	ds_read_b128 v[242:245], v213 offset:22528
	ds_read_b128 v[246:249], v213 offset:23040
	v_exp_f32_e32 v14, v14
	v_exp_f32_e32 v15, v15
	v_exp_f32_e32 v16, v16
	v_exp_f32_e32 v17, v17
	v_cvt_pk_bf16_f32 v164, v26, v27
	v_add_f32_e32 v22, v36, v2
	v_add_f32_e32 v22, v3, v22
	v_add_f32_e32 v22, v4, v22
	v_add_f32_e32 v36, v5, v22
	v_cvt_pk_bf16_f32 v165, v28, v29
	s_waitcnt lgkmcnt(5)
	v_mfma_f32_32x32x16_bf16 v[98:113], v[226:229], v[184:187], v[98:113]
	v_add_f32_e32 v36, v36, v6
	v_add_f32_e32 v36, v7, v36
	v_add_f32_e32 v36, v8, v36
	v_add_f32_e32 v36, v9, v36
	v_cvt_pk_bf16_f32 v166, v30, v31
	v_cvt_pk_bf16_f32 v167, v32, v33
	s_waitcnt lgkmcnt(4)
	v_mfma_f32_32x32x16_bf16 v[114:129], v[230:233], v[184:187], v[114:129]
	v_add_f32_e32 v18, v10, v36
	v_add_f32_e32 v18, v11, v18
	v_add_f32_e32 v18, v12, v18
	v_add_f32_e32 v36, v13, v18
	v_cvt_pk_bf16_f32 v168, v2, v3
	v_cvt_pk_bf16_f32 v169, v4, v5
	s_waitcnt lgkmcnt(3)
	v_mfma_f32_32x32x16_bf16 v[98:113], v[234:237], v[180:183], v[98:113]
	v_add_f32_e32 v2, v14, v36
	v_add_f32_e32 v2, v15, v2
	v_add_f32_e32 v2, v16, v2
	v_add_f32_e32 v2, v17, v2
	v_cvt_pk_bf16_f32 v170, v6, v7
	v_cvt_pk_bf16_f32 v171, v8, v9
	s_waitcnt lgkmcnt(2)
	v_mfma_f32_32x32x16_bf16 v[114:129], v[238:241], v[180:183], v[114:129]
	v_cvt_pk_bf16_f32 v172, v10, v11
	v_cvt_pk_bf16_f32 v173, v12, v13
	s_waitcnt lgkmcnt(1)
	v_mfma_f32_32x32x16_bf16 v[98:113], v[242:245], v[176:179], v[98:113]
	v_cvt_pk_bf16_f32 v174, v14, v15
	v_cvt_pk_bf16_f32 v175, v16, v17
	s_waitcnt lgkmcnt(0)
	v_mfma_f32_32x32x16_bf16 v[114:129], v[246:249], v[176:179], v[114:129]
	s_setprio 0
	v_lshl_add_u64 v[4:5], v[204:205], 0, s[22:23]
	s_mov_b32 s0, m0
	s_mov_b32 m0, s44
	s_nop 0
	global_load_lds_dwordx4 v[4:5], off
	s_mov_b32 m0, s0
	s_and_saveexec_b64 s[0:1], s[2:3]
	s_cbranch_execz .LBB0_1154
	v_lshl_add_u64 v[4:5], v[202:203], 0, s[26:27]
	s_mov_b32 s43, m0
	s_mov_b32 m0, s70
	s_nop 0
	global_load_lds_dwordx4 v[4:5], off
	s_mov_b32 m0, s43

.LBB0_1158:
	s_mov_b32 s79, s45
	s_waitcnt vmcnt(3) lgkmcnt(0)
	s_barrier
	s_mul_i32 s72, s79, 0x3000
	s_mov_b32 s45, s42
	v_add_u32_e32 v133, s72, v213
	s_setprio 1
	ds_read_b128 v[226:229], v133
	ds_read_b128 v[230:233], v133 offset:512
	ds_read_b128 v[234:237], v133 offset:2048
	ds_read_b128 v[238:241], v133 offset:2560
	ds_read_b128 v[242:245], v133 offset:4096
	ds_read_b128 v[246:249], v133 offset:4608
	v_exp_f32_e32 v66, v66
	v_exp_f32_e32 v67, v67
	v_exp_f32_e32 v68, v68
	v_exp_f32_e32 v69, v69
	s_nop 0
	v_exp_f32_e32 v70, v70
	v_exp_f32_e32 v71, v71
	v_exp_f32_e32 v72, v72
	v_exp_f32_e32 v73, v73
	s_waitcnt lgkmcnt(5)
	v_mfma_f32_32x32x16_bf16 v[98:113], v[226:229], v[196:199], v[34:49]
	v_exp_f32_e32 v74, v74
	v_exp_f32_e32 v75, v75
	v_exp_f32_e32 v76, v76
	v_exp_f32_e32 v77, v77
	s_waitcnt lgkmcnt(4)
	v_mfma_f32_32x32x16_bf16 v[82:97], v[230:233], v[196:199], v[34:49]
	ds_read_b128 v[226:229], v133 offset:6144
	ds_read_b128 v[230:233], v133 offset:6656
	v_exp_f32_e32 v78, v78
	v_exp_f32_e32 v79, v79
	v_exp_f32_e32 v80, v80
	v_exp_f32_e32 v81, v81
	s_nop 0
	v_add_f32_e32 v0, 0, v66
	v_add_f32_e32 v0, v67, v0
	v_add_f32_e32 v0, v68, v0
	v_add_f32_e32 v0, v69, v0
	s_waitcnt lgkmcnt(5)
	v_mfma_f32_32x32x16_bf16 v[98:113], v[234:237], v[192:195], v[98:113]
	v_add_f32_e32 v0, v0, v70
	v_add_f32_e32 v0, v71, v0
	v_add_f32_e32 v0, v72, v0
	v_exp_f32_e32 v50, v50
	v_exp_f32_e32 v51, v51
	v_exp_f32_e32 v52, v52
	v_exp_f32_e32 v53, v53
	v_add_f32_e32 v0, v73, v0
	s_waitcnt lgkmcnt(4)
	v_mfma_f32_32x32x16_bf16 v[82:97], v[238:241], v[192:195], v[82:97]
	ds_read_b128 v[234:237], v133 offset:8192
	ds_read_b128 v[238:241], v133 offset:8704
	v_add_f32_e32 v0, v74, v0
	v_add_f32_e32 v0, v75, v0
	v_add_f32_e32 v0, v76, v0
	v_exp_f32_e32 v54, v54
	v_exp_f32_e32 v55, v55
	v_exp_f32_e32 v56, v56
	v_exp_f32_e32 v57, v57
	v_add_f32_e32 v0, v77, v0
	v_cvt_pk_bf16_f32 v160, v66, v67
	v_cvt_pk_bf16_f32 v161, v68, v69
	s_waitcnt lgkmcnt(5)
	v_mfma_f32_32x32x16_bf16 v[98:113], v[242:245], v[188:191], v[98:113]
	v_add_f32_e32 v0, v78, v0
	v_add_f32_e32 v0, v79, v0
	v_add_f32_e32 v0, v80, v0
	v_exp_f32_e32 v58, v58
	v_exp_f32_e32 v59, v59
	v_exp_f32_e32 v60, v60
	v_exp_f32_e32 v61, v61
	v_add_f32_e32 v0, v81, v0
	v_cvt_pk_bf16_f32 v162, v70, v71
	v_cvt_pk_bf16_f32 v163, v72, v73
	s_waitcnt lgkmcnt(4)
	v_mfma_f32_32x32x16_bf16 v[82:97], v[246:249], v[188:191], v[82:97]
	ds_read_b128 v[242:245], v133 offset:10240
	ds_read_b128 v[246:249], v133 offset:10752
	v_exp_f32_e32 v62, v62
	v_exp_f32_e32 v63, v63
	v_exp_f32_e32 v64, v64
	v_exp_f32_e32 v65, v65
	v_cvt_pk_bf16_f32 v164, v74, v75
	v_add_f32_e32 v0, v0, v50
	v_add_f32_e32 v0, v51, v0
	v_add_f32_e32 v0, v52, v0
	v_add_f32_e32 v0, v53, v0
	v_cvt_pk_bf16_f32 v165, v76, v77
	s_waitcnt lgkmcnt(5)
	v_mfma_f32_32x32x16_bf16 v[98:113], v[226:229], v[184:187], v[98:113]
	v_add_f32_e32 v0, v0, v54
	v_add_f32_e32 v0, v55, v0
	v_add_f32_e32 v0, v56, v0
	v_add_f32_e32 v0, v57, v0
	v_cvt_pk_bf16_f32 v166, v78, v79
	v_cvt_pk_bf16_f32 v167, v80, v81
	s_waitcnt lgkmcnt(4)
	v_mfma_f32_32x32x16_bf16 v[82:97], v[230:233], v[184:187], v[82:97]
	v_add_f32_e32 v0, v58, v0
	v_add_f32_e32 v0, v59, v0
	v_add_f32_e32 v0, v60, v0
	v_add_f32_e32 v0, v61, v0
	v_cvt_pk_bf16_f32 v168, v50, v51
	v_cvt_pk_bf16_f32 v169, v52, v53
	s_waitcnt lgkmcnt(3)
	v_mfma_f32_32x32x16_bf16 v[98:113], v[234:237], v[180:183], v[98:113]
	v_add_f32_e32 v0, v62, v0
	v_add_f32_e32 v0, v63, v0
	v_add_f32_e32 v0, v64, v0
	v_add_f32_e32 v0, v65, v0
	v_cvt_pk_bf16_f32 v170, v54, v55
	v_cvt_pk_bf16_f32 v171, v56, v57
	s_waitcnt lgkmcnt(2)
	v_mfma_f32_32x32x16_bf16 v[82:97], v[238:241], v[180:183], v[82:97]
	v_cvt_pk_bf16_f32 v172, v58, v59
	v_cvt_pk_bf16_f32 v173, v60, v61
	s_waitcnt lgkmcnt(1)
	v_mfma_f32_32x32x16_bf16 v[98:113], v[242:245], v[176:179], v[98:113]
	v_cvt_pk_bf16_f32 v174, v62, v63
	v_cvt_pk_bf16_f32 v175, v64, v65
	s_waitcnt lgkmcnt(0)
	v_mfma_f32_32x32x16_bf16 v[82:97], v[246:249], v[176:179], v[82:97]
	s_setprio 0
	v_lshl_add_u64 v[116:117], v[204:205], 0, s[0:1]
	s_mul_i32 s76, s42, 0x3000
	v_lshl_add_u64 v[50:51], v[116:117], 0, s[12:13]
	s_add_i32 s46, s76, s44
	s_mov_b32 s42, m0
	s_mov_b32 m0, s46
	s_nop 0
	global_load_lds_dwordx4 v[50:51], off
	s_mov_b32 m0, s42
	s_and_saveexec_b64 s[42:43], s[2:3]
	s_cbranch_execz .LBB0_1160
	s_add_i32 s73, s76, s70
	v_lshl_add_u64 v[50:51], v[114:115], 0, s[30:31]
	s_mov_b32 s74, m0
	s_mov_b32 m0, s73
	s_nop 0
	global_load_lds_dwordx4 v[50:51], off
	s_mov_b32 m0, s74

.LBB0_1161:
	s_waitcnt vmcnt(3) lgkmcnt(0)
	s_barrier
	s_mul_i32 s82, s47, 0x3000
	v_add_u32_e32 v132, s82, v213
	s_setprio 1
	ds_read_b128 v[226:229], v132
	ds_read_b128 v[230:233], v132 offset:512
	ds_read_b128 v[234:237], v132 offset:2048
	ds_read_b128 v[238:241], v132 offset:2560
	ds_read_b128 v[242:245], v132 offset:4096
	ds_read_b128 v[246:249], v132 offset:4608
	v_exp_f32_e32 v98, v98
	v_exp_f32_e32 v99, v99
	v_exp_f32_e32 v100, v100
	v_exp_f32_e32 v101, v101
	s_nop 0
	v_exp_f32_e32 v102, v102
	v_exp_f32_e32 v103, v103
	v_exp_f32_e32 v104, v104
	v_exp_f32_e32 v105, v105
	s_waitcnt lgkmcnt(5)
	v_mfma_f32_32x32x16_bf16 v[66:81], v[226:229], v[196:199], v[34:49]
	v_exp_f32_e32 v106, v106
	v_exp_f32_e32 v107, v107
	v_exp_f32_e32 v108, v108
	v_exp_f32_e32 v109, v109
	s_waitcnt lgkmcnt(4)
	v_mfma_f32_32x32x16_bf16 v[50:65], v[230:233], v[196:199], v[34:49]
	ds_read_b128 v[226:229], v132 offset:6144
	ds_read_b128 v[230:233], v132 offset:6656
	v_exp_f32_e32 v110, v110
	v_exp_f32_e32 v111, v111
	v_exp_f32_e32 v112, v112
	v_exp_f32_e32 v113, v113
	s_nop 0
	v_add_f32_e32 v0, 0, v98
	v_add_f32_e32 v0, v99, v0
	v_add_f32_e32 v0, v100, v0
	v_add_f32_e32 v0, v101, v0
	s_waitcnt lgkmcnt(5)
	v_mfma_f32_32x32x16_bf16 v[66:81], v[234:237], v[192:195], v[66:81]
	v_add_f32_e32 v0, v0, v102
	v_add_f32_e32 v0, v103, v0
	v_add_f32_e32 v0, v104, v0
	v_exp_f32_e32 v82, v82
	v_exp_f32_e32 v83, v83
	v_exp_f32_e32 v84, v84
	v_exp_f32_e32 v85, v85
	v_add_f32_e32 v0, v105, v0
	s_waitcnt lgkmcnt(4)
	v_mfma_f32_32x32x16_bf16 v[50:65], v[238:241], v[192:195], v[50:65]
	ds_read_b128 v[234:237], v132 offset:8192
	ds_read_b128 v[238:241], v132 offset:8704
	v_add_f32_e32 v0, v106, v0
	v_add_f32_e32 v0, v107, v0
	v_add_f32_e32 v0, v108, v0
	v_exp_f32_e32 v86, v86
	v_exp_f32_e32 v87, v87
	v_exp_f32_e32 v88, v88
	v_exp_f32_e32 v89, v89
	v_add_f32_e32 v0, v109, v0
	v_cvt_pk_bf16_f32 v160, v98, v99
	v_cvt_pk_bf16_f32 v161, v100, v101
	s_waitcnt lgkmcnt(5)
	v_mfma_f32_32x32x16_bf16 v[66:81], v[242:245], v[188:191], v[66:81]
	v_add_f32_e32 v0, v110, v0
	v_add_f32_e32 v0, v111, v0
	v_add_f32_e32 v0, v112, v0
	v_exp_f32_e32 v90, v90
	v_exp_f32_e32 v91, v91
	v_exp_f32_e32 v92, v92
	v_exp_f32_e32 v93, v93
	v_add_f32_e32 v0, v113, v0
	v_cvt_pk_bf16_f32 v162, v102, v103
	v_cvt_pk_bf16_f32 v163, v104, v105
	s_waitcnt lgkmcnt(4)
	v_mfma_f32_32x32x16_bf16 v[50:65], v[246:249], v[188:191], v[50:65]
	ds_read_b128 v[242:245], v132 offset:10240
	ds_read_b128 v[246:249], v132 offset:10752
	v_exp_f32_e32 v94, v94
	v_exp_f32_e32 v95, v95
	v_exp_f32_e32 v96, v96
	v_exp_f32_e32 v97, v97
	v_cvt_pk_bf16_f32 v164, v106, v107
	v_add_f32_e32 v0, v0, v82
	v_add_f32_e32 v0, v83, v0
	v_add_f32_e32 v0, v84, v0
	v_add_f32_e32 v0, v85, v0
	v_cvt_pk_bf16_f32 v165, v108, v109
	s_waitcnt lgkmcnt(5)
	v_mfma_f32_32x32x16_bf16 v[66:81], v[226:229], v[184:187], v[66:81]
	v_add_f32_e32 v0, v0, v86
	v_add_f32_e32 v0, v87, v0
	v_add_f32_e32 v0, v88, v0
	v_add_f32_e32 v0, v89, v0
	v_cvt_pk_bf16_f32 v166, v110, v111
	v_cvt_pk_bf16_f32 v167, v112, v113
	s_waitcnt lgkmcnt(4)
	v_mfma_f32_32x32x16_bf16 v[50:65], v[230:233], v[184:187], v[50:65]
	v_add_f32_e32 v0, v90, v0
	v_add_f32_e32 v0, v91, v0
	v_add_f32_e32 v0, v92, v0
	v_add_f32_e32 v0, v93, v0
	v_cvt_pk_bf16_f32 v168, v82, v83
	v_cvt_pk_bf16_f32 v169, v84, v85
	s_waitcnt lgkmcnt(3)
	v_mfma_f32_32x32x16_bf16 v[66:81], v[234:237], v[180:183], v[66:81]
	v_add_f32_e32 v0, v94, v0
	v_add_f32_e32 v0, v95, v0
	v_add_f32_e32 v0, v96, v0
	v_add_f32_e32 v0, v97, v0
	v_cvt_pk_bf16_f32 v170, v86, v87
	v_cvt_pk_bf16_f32 v171, v88, v89
	s_waitcnt lgkmcnt(2)
	v_mfma_f32_32x32x16_bf16 v[50:65], v[238:241], v[180:183], v[50:65]
	v_cvt_pk_bf16_f32 v172, v90, v91
	v_cvt_pk_bf16_f32 v173, v92, v93
	s_waitcnt lgkmcnt(1)
	v_mfma_f32_32x32x16_bf16 v[66:81], v[242:245], v[176:179], v[66:81]
	v_cvt_pk_bf16_f32 v174, v94, v95
	v_cvt_pk_bf16_f32 v175, v96, v97
	s_waitcnt lgkmcnt(0)
	v_mfma_f32_32x32x16_bf16 v[50:65], v[246:249], v[176:179], v[50:65]
	s_setprio 0
	v_lshl_add_u64 v[82:83], v[116:117], 0, s[18:19]
	s_add_i32 s42, s72, s44
	s_mov_b32 s43, m0
	s_mov_b32 m0, s42
	s_nop 0
	global_load_lds_dwordx4 v[82:83], off
	s_mov_b32 m0, s43
	s_and_saveexec_b64 s[42:43], s[2:3]
	s_cbranch_execz .LBB0_1163
	s_add_i32 s72, s72, s70
	s_mov_b32 s77, m0
	s_mov_b32 m0, s72
	s_nop 0
	global_load_lds_dwordx4 v[114:115], off
	s_mov_b32 m0, s77

.LBB0_1173:
	s_waitcnt vmcnt(3) lgkmcnt(0)
	s_barrier
	v_add_u32_e32 v130, s76, v213
	s_setprio 1
	ds_read_b128 v[226:229], v130
	ds_read_b128 v[230:233], v130 offset:512
	ds_read_b128 v[234:237], v130 offset:2048
	ds_read_b128 v[238:241], v130 offset:2560
	ds_read_b128 v[242:245], v130 offset:4096
	ds_read_b128 v[246:249], v130 offset:4608
	v_exp_f32_e32 v66, v66
	v_exp_f32_e32 v67, v67
	v_exp_f32_e32 v68, v68
	v_exp_f32_e32 v69, v69
	s_nop 0
	v_exp_f32_e32 v70, v70
	v_exp_f32_e32 v71, v71
	v_exp_f32_e32 v72, v72
	v_exp_f32_e32 v73, v73
	s_waitcnt lgkmcnt(5)
	v_mfma_f32_32x32x16_bf16 v[82:97], v[226:229], v[196:199], v[34:49]
	v_exp_f32_e32 v74, v74
	v_exp_f32_e32 v75, v75
	v_exp_f32_e32 v76, v76
	v_exp_f32_e32 v77, v77
	s_waitcnt lgkmcnt(4)
	v_mfma_f32_32x32x16_bf16 v[98:113], v[230:233], v[196:199], v[34:49]
	ds_read_b128 v[226:229], v130 offset:6144
	ds_read_b128 v[230:233], v130 offset:6656
	v_exp_f32_e32 v78, v78
	v_exp_f32_e32 v79, v79
	v_exp_f32_e32 v80, v80
	v_exp_f32_e32 v81, v81
	s_nop 0
	v_add_f32_e32 v0, 0, v66
	v_add_f32_e32 v0, v67, v0
	v_add_f32_e32 v0, v68, v0
	v_add_f32_e32 v0, v69, v0
	s_waitcnt lgkmcnt(5)
	v_mfma_f32_32x32x16_bf16 v[82:97], v[234:237], v[192:195], v[82:97]
	v_add_f32_e32 v0, v0, v70
	v_add_f32_e32 v0, v71, v0
	v_add_f32_e32 v0, v72, v0
	v_exp_f32_e32 v50, v50
	v_exp_f32_e32 v51, v51
	v_exp_f32_e32 v52, v52
	v_exp_f32_e32 v53, v53
	v_add_f32_e32 v0, v73, v0
	s_waitcnt lgkmcnt(4)
	v_mfma_f32_32x32x16_bf16 v[98:113], v[238:241], v[192:195], v[98:113]
	ds_read_b128 v[234:237], v130 offset:8192
	ds_read_b128 v[238:241], v130 offset:8704
	v_add_f32_e32 v0, v74, v0
	v_add_f32_e32 v0, v75, v0
	v_add_f32_e32 v0, v76, v0
	v_exp_f32_e32 v54, v54
	v_exp_f32_e32 v55, v55
	v_exp_f32_e32 v56, v56
	v_exp_f32_e32 v57, v57
	v_add_f32_e32 v0, v77, v0
	v_cvt_pk_bf16_f32 v160, v66, v67
	v_cvt_pk_bf16_f32 v161, v68, v69
	s_waitcnt lgkmcnt(5)
	v_mfma_f32_32x32x16_bf16 v[82:97], v[242:245], v[188:191], v[82:97]
	v_add_f32_e32 v0, v78, v0
	v_add_f32_e32 v0, v79, v0
	v_add_f32_e32 v0, v80, v0
	v_exp_f32_e32 v58, v58
	v_exp_f32_e32 v59, v59
	v_exp_f32_e32 v60, v60
	v_exp_f32_e32 v61, v61
	v_add_f32_e32 v0, v81, v0
	v_cvt_pk_bf16_f32 v162, v70, v71
	v_cvt_pk_bf16_f32 v163, v72, v73
	s_waitcnt lgkmcnt(4)
	v_mfma_f32_32x32x16_bf16 v[98:113], v[246:249], v[188:191], v[98:113]
	ds_read_b128 v[242:245], v130 offset:10240
	ds_read_b128 v[246:249], v130 offset:10752
	v_exp_f32_e32 v62, v62
	v_exp_f32_e32 v63, v63
	v_exp_f32_e32 v64, v64
	v_exp_f32_e32 v65, v65
	v_cvt_pk_bf16_f32 v164, v74, v75
	v_add_f32_e32 v0, v0, v50
	v_add_f32_e32 v0, v51, v0
	v_add_f32_e32 v0, v52, v0
	v_add_f32_e32 v0, v53, v0
	v_cvt_pk_bf16_f32 v165, v76, v77
	s_waitcnt lgkmcnt(5)
	v_mfma_f32_32x32x16_bf16 v[82:97], v[226:229], v[184:187], v[82:97]
	v_add_f32_e32 v0, v0, v54
	v_add_f32_e32 v0, v55, v0
	v_add_f32_e32 v0, v56, v0
	v_add_f32_e32 v0, v57, v0
	v_cvt_pk_bf16_f32 v166, v78, v79
	v_cvt_pk_bf16_f32 v167, v80, v81
	s_waitcnt lgkmcnt(4)
	v_mfma_f32_32x32x16_bf16 v[98:113], v[230:233], v[184:187], v[98:113]
	v_add_f32_e32 v0, v58, v0
	v_add_f32_e32 v0, v59, v0
	v_add_f32_e32 v0, v60, v0
	v_add_f32_e32 v0, v61, v0
	v_cvt_pk_bf16_f32 v168, v50, v51
	v_cvt_pk_bf16_f32 v169, v52, v53
	s_waitcnt lgkmcnt(3)
	v_mfma_f32_32x32x16_bf16 v[82:97], v[234:237], v[180:183], v[82:97]
	v_add_f32_e32 v0, v62, v0
	v_add_f32_e32 v0, v63, v0
	v_add_f32_e32 v0, v64, v0
	v_add_f32_e32 v0, v65, v0
	v_cvt_pk_bf16_f32 v170, v54, v55
	v_cvt_pk_bf16_f32 v171, v56, v57
	s_waitcnt lgkmcnt(2)
	v_mfma_f32_32x32x16_bf16 v[98:113], v[238:241], v[180:183], v[98:113]
	v_cvt_pk_bf16_f32 v172, v58, v59
	v_cvt_pk_bf16_f32 v173, v60, v61
	s_waitcnt lgkmcnt(1)
	v_mfma_f32_32x32x16_bf16 v[82:97], v[242:245], v[176:179], v[82:97]
	v_cvt_pk_bf16_f32 v174, v62, v63
	v_cvt_pk_bf16_f32 v175, v64, v65
	s_waitcnt lgkmcnt(0)
	v_mfma_f32_32x32x16_bf16 v[98:113], v[246:249], v[176:179], v[98:113]
	s_setprio 0
	s_add_i32 s10, s81, 5
	s_lshl_b64 s[42:43], s[10:11], 17
	v_lshl_add_u64 v[50:51], v[204:205], 0, s[42:43]
	s_add_i32 s44, s82, s44
	s_mov_b32 s45, m0
	s_mov_b32 m0, s44
	s_nop 0
	global_load_lds_dwordx4 v[50:51], off
	s_mov_b32 m0, s45
	s_and_saveexec_b64 s[44:45], s[2:3]
	s_cbranch_execz .LBB0_1175
	s_lshl_b64 s[78:79], s[10:11], 12
	s_add_i32 s47, s82, s70
	v_lshl_add_u64 v[50:51], v[202:203], 0, s[78:79]
	s_mov_b32 s78, m0
	s_mov_b32 m0, s47
	s_nop 0
	global_load_lds_dwordx4 v[50:51], off
	s_mov_b32 m0, s78

.LBB0_1176:
	s_waitcnt vmcnt(3) lgkmcnt(0)
	s_barrier
	s_setprio 1
	ds_read_b128 v[226:229], v133
	ds_read_b128 v[230:233], v133 offset:512
	ds_read_b128 v[234:237], v133 offset:2048
	ds_read_b128 v[238:241], v133 offset:2560
	ds_read_b128 v[242:245], v133 offset:4096
	ds_read_b128 v[246:249], v133 offset:4608
	v_exp_f32_e32 v66, v66
	v_exp_f32_e32 v67, v67
	v_exp_f32_e32 v68, v68
	v_exp_f32_e32 v69, v69
	s_nop 0
	v_exp_f32_e32 v70, v70
	v_exp_f32_e32 v71, v71
	v_exp_f32_e32 v72, v72
	v_exp_f32_e32 v73, v73
	s_waitcnt lgkmcnt(5)
	v_mfma_f32_32x32x16_bf16 v[82:97], v[226:229], v[196:199], v[34:49]
	v_exp_f32_e32 v74, v74
	v_exp_f32_e32 v75, v75
	v_exp_f32_e32 v76, v76
	v_exp_f32_e32 v77, v77
	s_waitcnt lgkmcnt(4)
	v_mfma_f32_32x32x16_bf16 v[98:113], v[230:233], v[196:199], v[34:49]
	ds_read_b128 v[226:229], v133 offset:6144
	ds_read_b128 v[230:233], v133 offset:6656
	v_exp_f32_e32 v78, v78
	v_exp_f32_e32 v79, v79
	v_exp_f32_e32 v80, v80
	v_exp_f32_e32 v81, v81
	s_nop 0
	v_add_f32_e32 v0, 0, v66
	v_add_f32_e32 v0, v67, v0
	v_add_f32_e32 v0, v68, v0
	v_add_f32_e32 v0, v69, v0
	s_waitcnt lgkmcnt(5)
	v_mfma_f32_32x32x16_bf16 v[82:97], v[234:237], v[192:195], v[82:97]
	v_add_f32_e32 v0, v0, v70
	v_add_f32_e32 v0, v71, v0
	v_add_f32_e32 v0, v72, v0
	v_exp_f32_e32 v50, v50
	v_exp_f32_e32 v51, v51
	v_exp_f32_e32 v52, v52
	v_exp_f32_e32 v53, v53
	v_add_f32_e32 v0, v73, v0
	s_waitcnt lgkmcnt(4)
	v_mfma_f32_32x32x16_bf16 v[98:113], v[238:241], v[192:195], v[98:113]
	ds_read_b128 v[234:237], v133 offset:8192
	ds_read_b128 v[238:241], v133 offset:8704
	v_add_f32_e32 v0, v74, v0
	v_add_f32_e32 v0, v75, v0
	v_add_f32_e32 v0, v76, v0
	v_exp_f32_e32 v54, v54
	v_exp_f32_e32 v55, v55
	v_exp_f32_e32 v56, v56
	v_exp_f32_e32 v57, v57
	v_add_f32_e32 v0, v77, v0
	v_cvt_pk_bf16_f32 v160, v66, v67
	v_cvt_pk_bf16_f32 v161, v68, v69
	s_waitcnt lgkmcnt(5)
	v_mfma_f32_32x32x16_bf16 v[82:97], v[242:245], v[188:191], v[82:97]
	v_add_f32_e32 v0, v78, v0
	v_add_f32_e32 v0, v79, v0
	v_add_f32_e32 v0, v80, v0
	v_exp_f32_e32 v58, v58
	v_exp_f32_e32 v59, v59
	v_exp_f32_e32 v60, v60
	v_exp_f32_e32 v61, v61
	v_add_f32_e32 v0, v81, v0
	v_cvt_pk_bf16_f32 v162, v70, v71
	v_cvt_pk_bf16_f32 v163, v72, v73
	s_waitcnt lgkmcnt(4)
	v_mfma_f32_32x32x16_bf16 v[98:113], v[246:249], v[188:191], v[98:113]
	ds_read_b128 v[242:245], v133 offset:10240
	ds_read_b128 v[246:249], v133 offset:10752
	v_exp_f32_e32 v62, v62
	v_exp_f32_e32 v63, v63
	v_exp_f32_e32 v64, v64
	v_exp_f32_e32 v65, v65
	v_cvt_pk_bf16_f32 v164, v74, v75
	v_add_f32_e32 v0, v0, v50
	v_add_f32_e32 v0, v51, v0
	v_add_f32_e32 v0, v52, v0
	v_add_f32_e32 v0, v53, v0
	v_cvt_pk_bf16_f32 v165, v76, v77
	s_waitcnt lgkmcnt(5)
	v_mfma_f32_32x32x16_bf16 v[82:97], v[226:229], v[184:187], v[82:97]
	v_add_f32_e32 v0, v0, v54
	v_add_f32_e32 v0, v55, v0
	v_add_f32_e32 v0, v56, v0
	v_add_f32_e32 v0, v57, v0
	v_cvt_pk_bf16_f32 v166, v78, v79
	v_cvt_pk_bf16_f32 v167, v80, v81
	s_waitcnt lgkmcnt(4)
	v_mfma_f32_32x32x16_bf16 v[98:113], v[230:233], v[184:187], v[98:113]
	v_add_f32_e32 v0, v58, v0
	v_add_f32_e32 v0, v59, v0
	v_add_f32_e32 v0, v60, v0
	v_add_f32_e32 v0, v61, v0
	v_cvt_pk_bf16_f32 v168, v50, v51
	v_cvt_pk_bf16_f32 v169, v52, v53
	s_waitcnt lgkmcnt(3)
	v_mfma_f32_32x32x16_bf16 v[82:97], v[234:237], v[180:183], v[82:97]
	v_add_f32_e32 v0, v62, v0
	v_add_f32_e32 v0, v63, v0
	v_add_f32_e32 v0, v64, v0
	v_add_f32_e32 v0, v65, v0
	v_cvt_pk_bf16_f32 v170, v54, v55
	v_cvt_pk_bf16_f32 v171, v56, v57
	s_waitcnt lgkmcnt(2)
	v_mfma_f32_32x32x16_bf16 v[98:113], v[238:241], v[180:183], v[98:113]
	v_cvt_pk_bf16_f32 v172, v58, v59
	v_cvt_pk_bf16_f32 v173, v60, v61
	s_waitcnt lgkmcnt(1)
	v_mfma_f32_32x32x16_bf16 v[82:97], v[242:245], v[176:179], v[82:97]
	v_cvt_pk_bf16_f32 v174, v62, v63
	v_cvt_pk_bf16_f32 v175, v64, v65
	s_waitcnt lgkmcnt(0)
	v_mfma_f32_32x32x16_bf16 v[98:113], v[246:249], v[176:179], v[98:113]
	s_setprio 0
	s_add_i32 s44, s81, 6
	s_mov_b32 s45, s11
	s_lshl_b64 s[0:1], s[44:45], 17
	v_lshl_add_u64 v[50:51], v[204:205], 0, s[0:1]
	s_mov_b32 s47, m0
	s_mov_b32 m0, s46
	s_nop 0
	global_load_lds_dwordx4 v[50:51], off
	s_mov_b32 m0, s47
	s_and_saveexec_b64 s[46:47], s[2:3]
	s_cbranch_execz .LBB0_1178
	s_lshl_b64 s[44:45], s[44:45], 12
	s_add_i32 s70, s76, s70
	v_lshl_add_u64 v[50:51], v[202:203], 0, s[44:45]
	s_mov_b32 s44, m0
	s_mov_b32 m0, s70
	s_nop 0
	global_load_lds_dwordx4 v[50:51], off
	s_mov_b32 m0, s44

; __device__ __forceinline__ void pv(f32x16* o, int vb, bf16x8 pa0, bf16x8 pa1, bf16x8 pa2, bf16x8 pa3) {
; #pragma unroll
;     for (int d0 = 0; d0 < 2; ++d0) { s16x4 lo[4], hi[4];
; #pragma unroll
;         for (int ks = 0; ks < 4; ++ks) {
;             asm volatile("ds_read_b64_tr_b16 %0,%1 offset:%c2" : "=&v"(lo[ks]) : "v"(vb), "i"(d0 * 4096 + ks * 1024) : "memory");
;             asm volatile("ds_read_b64_tr_b16 %0,%1 offset:%c2" : "=&v"(hi[ks]) : "v"(vb), "i"(d0 * 4096 + ks * 1024 + 512) : "memory"); }
;         asm volatile("s_waitcnt lgkmcnt(0)" ::: "memory"); __builtin_amdgcn_sched_barrier(0);
;     ...
;         o[d0] = __builtin_amdgcn_mfma_f32_32x32x16_bf16(pa0, MLA_PK(0), o[d0], 0, 0, 0);
;         o[d0] = __builtin_amdgcn_mfma_f32_32x32x16_bf16(pa1, MLA_PK(1), o[d0], 0, 0, 0);
;         o[d0] = __builtin_amdgcn_mfma_f32_32x32x16_bf16(pa2, MLA_PK(2), o[d0], 0, 0, 0);
;         o[d0] = __builtin_amdgcn_mfma_f32_32x32x16_bf16(pa3, MLA_PK(3), o[d0], 0, 0, 0);
;     ...
;     }
; }
.LBB0_1179:
	s_waitcnt vmcnt(3) lgkmcnt(0)
	s_barrier
	s_setprio 1
	ds_read_b128 v[226:229], v132
	ds_read_b128 v[230:233], v132 offset:512
	ds_read_b128 v[234:237], v132 offset:2048
	ds_read_b128 v[238:241], v132 offset:2560
	ds_read_b128 v[242:245], v132 offset:4096
	ds_read_b128 v[246:249], v132 offset:4608
	v_exp_f32_e32 v66, v66
	v_exp_f32_e32 v67, v67
	v_exp_f32_e32 v68, v68
	v_exp_f32_e32 v69, v69
	s_nop 0
	v_exp_f32_e32 v70, v70
	v_exp_f32_e32 v71, v71
	v_exp_f32_e32 v72, v72
	v_exp_f32_e32 v73, v73
	v_exp_f32_e32 v74, v74
	v_exp_f32_e32 v75, v75
	v_exp_f32_e32 v76, v76
	v_exp_f32_e32 v77, v77
	s_waitcnt lgkmcnt(5)
	v_mfma_f32_32x32x16_bf16 v[82:97], v[226:229], v[196:199], v[34:49]
	s_nop 0
	v_exp_f32_e32 v78, v78
	v_exp_f32_e32 v79, v79
	v_exp_f32_e32 v80, v80
	v_exp_f32_e32 v81, v81
	s_waitcnt lgkmcnt(4)
	v_mfma_f32_32x32x16_bf16 v[98:113], v[230:233], v[196:199], v[34:49]
	ds_read_b128 v[226:229], v132 offset:6144
	ds_read_b128 v[230:233], v132 offset:6656
	v_add_f32_e32 v0, 0, v66
	v_add_f32_e32 v0, v67, v0
	v_add_f32_e32 v0, v68, v0
	v_add_f32_e32 v0, v69, v0
	v_add_f32_e32 v0, v0, v70
	v_add_f32_e32 v0, v71, v0
	v_add_f32_e32 v0, v72, v0
	v_exp_f32_e32 v50, v50
	v_exp_f32_e32 v51, v51
	v_exp_f32_e32 v52, v52
	v_exp_f32_e32 v53, v53
	v_add_f32_e32 v0, v73, v0
	s_waitcnt lgkmcnt(5)
	v_mfma_f32_32x32x16_bf16 v[82:97], v[234:237], v[192:195], v[82:97]
	s_nop 0
	v_add_f32_e32 v0, v74, v0
	v_add_f32_e32 v0, v75, v0
	v_add_f32_e32 v0, v76, v0
	v_exp_f32_e32 v54, v54
	v_exp_f32_e32 v55, v55
	v_exp_f32_e32 v56, v56
	v_exp_f32_e32 v57, v57
	v_add_f32_e32 v0, v77, v0
	v_cvt_pk_bf16_f32 v160, v66, v67
	v_cvt_pk_bf16_f32 v161, v68, v69
	s_waitcnt lgkmcnt(4)
	v_mfma_f32_32x32x16_bf16 v[98:113], v[238:241], v[192:195], v[98:113]
	ds_read_b128 v[234:237], v132 offset:8192
	ds_read_b128 v[238:241], v132 offset:8704
	v_add_f32_e32 v0, v78, v0
	v_add_f32_e32 v0, v79, v0
	v_add_f32_e32 v0, v80, v0
	v_exp_f32_e32 v58, v58
	v_exp_f32_e32 v59, v59
	v_exp_f32_e32 v60, v60
	v_exp_f32_e32 v61, v61
	v_add_f32_e32 v0, v81, v0
	v_cvt_pk_bf16_f32 v162, v70, v71
	v_cvt_pk_bf16_f32 v163, v72, v73
	s_waitcnt lgkmcnt(5)
	v_mfma_f32_32x32x16_bf16 v[82:97], v[242:245], v[188:191], v[82:97]
	s_nop 0
	v_exp_f32_e32 v62, v62
	v_exp_f32_e32 v63, v63
	v_exp_f32_e32 v64, v64
	v_exp_f32_e32 v65, v65
	v_cvt_pk_bf16_f32 v164, v74, v75
	v_add_f32_e32 v0, v0, v50
	v_add_f32_e32 v0, v51, v0
	v_add_f32_e32 v0, v52, v0
	v_add_f32_e32 v0, v53, v0
	v_cvt_pk_bf16_f32 v165, v76, v77
	s_waitcnt lgkmcnt(4)
	v_mfma_f32_32x32x16_bf16 v[98:113], v[246:249], v[188:191], v[98:113]
	ds_read_b128 v[242:245], v132 offset:10240
	ds_read_b128 v[246:249], v132 offset:10752
	v_add_f32_e32 v0, v0, v54
	v_add_f32_e32 v0, v55, v0
	v_add_f32_e32 v0, v56, v0
	v_add_f32_e32 v0, v57, v0
	v_cvt_pk_bf16_f32 v166, v78, v79
	v_cvt_pk_bf16_f32 v167, v80, v81
	s_waitcnt lgkmcnt(5)
	v_mfma_f32_32x32x16_bf16 v[82:97], v[226:229], v[184:187], v[82:97]
	s_nop 0
	v_add_f32_e32 v0, v58, v0
	v_add_f32_e32 v0, v59, v0
	v_add_f32_e32 v0, v60, v0
	v_add_f32_e32 v0, v61, v0
	v_cvt_pk_bf16_f32 v168, v50, v51
	v_cvt_pk_bf16_f32 v169, v52, v53
	s_waitcnt lgkmcnt(4)
	v_mfma_f32_32x32x16_bf16 v[98:113], v[230:233], v[184:187], v[98:113]
	v_add_f32_e32 v0, v62, v0
	v_add_f32_e32 v0, v63, v0
	v_add_f32_e32 v0, v64, v0
	v_add_f32_e32 v0, v65, v0
	v_cvt_pk_bf16_f32 v170, v54, v55
	v_cvt_pk_bf16_f32 v171, v56, v57
	s_waitcnt lgkmcnt(3)
	v_mfma_f32_32x32x16_bf16 v[82:97], v[234:237], v[180:183], v[82:97]
	v_cvt_pk_bf16_f32 v172, v58, v59
	v_cvt_pk_bf16_f32 v173, v60, v61
	s_waitcnt lgkmcnt(2)
	v_mfma_f32_32x32x16_bf16 v[98:113], v[238:241], v[180:183], v[98:113]
	v_cvt_pk_bf16_f32 v174, v62, v63
	v_cvt_pk_bf16_f32 v175, v64, v65
	s_waitcnt lgkmcnt(1)
	v_mfma_f32_32x32x16_bf16 v[82:97], v[242:245], v[176:179], v[82:97]
	s_waitcnt lgkmcnt(0)
	v_mfma_f32_32x32x16_bf16 v[98:113], v[246:249], v[176:179], v[98:113]
	v_add_f32_e32 v132, v133, v0
	s_setprio 0
	v_lshl_add_u64 v[50:51], v[200:201], 0, s[0:1]
	s_mov_b32 s0, m0
	s_mov_b32 m0, s74
	s_nop 0
	global_load_lds_dwordx4 v[50:51], off
	s_mov_b32 m0, s0
	s_xor_b32 s0, s73, 0x4000
	v_add_u32_e32 v0, s0, v211
	ds_read_b64_tr_b16 v[50:51],v0 offset:0
	ds_read_b64_tr_b16 v[52:53],v0 offset:512
	ds_read_b64_tr_b16 v[54:55],v0 offset:1024
	ds_read_b64_tr_b16 v[56:57],v0 offset:1536
	ds_read_b64_tr_b16 v[58:59],v0 offset:2048
	ds_read_b64_tr_b16 v[60:61],v0 offset:2560
	ds_read_b64_tr_b16 v[62:63],v0 offset:3072
	ds_read_b64_tr_b16 v[64:65],v0 offset:3584
	s_waitcnt lgkmcnt(0)
	s_nop 0
	v_mfma_f32_32x32x16_bf16 v[2:17], v[160:163], v[50:53], v[2:17]
	ds_read_b64_tr_b16 v[52:53],v0 offset:4096
	v_mfma_f32_32x32x16_bf16 v[2:17], v[164:167], v[54:57], v[2:17]
	ds_read_b64_tr_b16 v[54:55],v0 offset:4608
	ds_read_b64_tr_b16 v[56:57],v0 offset:5120
	v_mfma_f32_32x32x16_bf16 v[2:17], v[168:171], v[58:61], v[2:17]
	ds_read_b64_tr_b16 v[58:59],v0 offset:5632
	ds_read_b64_tr_b16 v[70:71],v0 offset:6144
	ds_read_b64_tr_b16 v[72:73],v0 offset:6656
	ds_read_b64_tr_b16 v[74:75],v0 offset:7168
	ds_read_b64_tr_b16 v[76:77],v0 offset:7680
	s_waitcnt lgkmcnt(0)
; __device__ __forceinline__ float max3f(float a, float b, float c) { float r; asm("v_max3_f32 %0, %1, %2, %3" : "=v"(r) : "v"(a), "v"(b), "v"(c)); return r; }
; __device__ __forceinline__ void cmask(f32x16& p0, f32x16& p1, int jb, int qrel, int hi) {
;     const float NEG = -INFINITY; const int kb = 64 * jb + 4 * hi;
; #pragma unroll
;     for (int r = 0; r < 16; ++r) { const int kv = kb + (r & 3) + 8 * (r >> 2); if (kv > qrel) p0[r] = NEG; if (kv + 32 > qrel) p1[r] = NEG; }
; }
; __device__ __forceinline__ float rowmax(const f32x16& p0, const f32x16& p1) {
;     float a = max3f(p0[0], p0[1], p1[0]), b = max3f(p0[2], p0[3], p1[1]); a = max3f(a, p1[2], p1[3]);
; #pragma unroll
;     for (int r = 4; r < 16; r += 4) { a = max3f(a, p0[r], p0[r + 1]); b = max3f(b, p0[r + 2], p0[r + 3]); a = max3f(a, p1[r], p1[r + 1]); b = max3f(b, p1[r + 2], p1[r + 3]); }
;     const float m = fmaxf(a, b);
;     auto rr = __builtin_amdgcn_permlane32_swap(__float_as_uint(m), __float_as_uint(m), false, false);
;     return fmaxf(__uint_as_float(rr[0]), __uint_as_float(rr[1]));
; }
; __device__ __forceinline__ void pv(f32x16* o, int vb, bf16x8 pa0, bf16x8 pa1, bf16x8 pa2, bf16x8 pa3) {
; #pragma unroll
;     for (int d0 = 0; d0 < 2; ++d0) { s16x4 lo[4], hi[4];
; #pragma unroll
;         for (int ks = 0; ks < 4; ++ks) {
;             asm volatile("ds_read_b64_tr_b16 %0,%1 offset:%c2" : "=&v"(lo[ks]) : "v"(vb), "i"(d0 * 4096 + ks * 1024) : "memory");
;             asm volatile("ds_read_b64_tr_b16 %0,%1 offset:%c2" : "=&v"(hi[ks]) : "v"(vb), "i"(d0 * 4096 + ks * 1024 + 512) : "memory"); }
;         asm volatile("s_waitcnt lgkmcnt(0)" ::: "memory"); __builtin_amdgcn_sched_barrier(0);
;     ...
;         o[d0] = __builtin_amdgcn_mfma_f32_32x32x16_bf16(pa0, MLA_PK(0), o[d0], 0, 0, 0);
;         o[d0] = __builtin_amdgcn_mfma_f32_32x32x16_bf16(pa1, MLA_PK(1), o[d0], 0, 0, 0);
;         o[d0] = __builtin_amdgcn_mfma_f32_32x32x16_bf16(pa2, MLA_PK(2), o[d0], 0, 0, 0);
;         o[d0] = __builtin_amdgcn_mfma_f32_32x32x16_bf16(pa3, MLA_PK(3), o[d0], 0, 0, 0);
;     ...
;     }
; }
	v_mfma_f32_32x32x16_bf16 v[2:17], v[172:175], v[62:65], v[2:17]
	v_mfma_f32_32x32x16_bf16 v[18:33], v[160:163], v[52:55], v[18:33]
	v_or_b32_e32 v50, 0xa0, v129
	v_or_b32_e32 v0, 0x80, v129
	v_cmp_le_i32_e32 vcc, v50, v131
	s_nop 1
	v_cndmask_b32_e32 v50, v206, v98, vcc
	v_cmp_lt_i32_e32 vcc, v0, v131
	v_mfma_f32_32x32x16_bf16 v[18:33], v[164:167], v[56:59], v[18:33]
	s_nop 0
	v_cndmask_b32_e32 v67, v206, v83, vcc
	v_cmp_le_i32_e32 vcc, v0, v131
	v_or_b32_e32 v0, 0xa1, v129
	s_nop 0
	v_cndmask_b32_e32 v66, v206, v82, vcc
	v_cmp_le_i32_e32 vcc, v0, v131
	v_or_b32_e32 v0, 0x82, v129
	v_mfma_f32_32x32x16_bf16 v[18:33], v[168:171], v[70:73], v[18:33]
	v_cndmask_b32_e32 v51, v206, v99, vcc
	v_cmp_le_i32_e32 vcc, v0, v131
	v_or_b32_e32 v0, 0xa2, v129
	s_nop 0
	v_cndmask_b32_e32 v68, v206, v84, vcc
	v_cmp_le_i32_e32 vcc, v0, v131
	v_or_b32_e32 v0, 0x83, v129
	v_mfma_f32_32x32x16_bf16 v[18:33], v[172:175], v[74:77], v[18:33]
	v_cndmask_b32_e32 v52, v206, v100, vcc
	v_cmp_le_i32_e32 vcc, v0, v131
	v_or_b32_e32 v0, 0xa3, v129
	s_nop 0
	v_cndmask_b32_e32 v69, v206, v85, vcc
	v_cmp_le_i32_e32 vcc, v0, v131
	v_or_b32_e32 v0, 0x88, v129
	v_max3_f32 v82, v68, v69, v51
	s_nop 0
	v_cndmask_b32_e32 v53, v206, v101, vcc
	v_cmp_le_i32_e32 vcc, v0, v131
	v_or_b32_e32 v0, 0xa8, v129
	s_nop 0
	v_cndmask_b32_e32 v70, v206, v86, vcc
	v_cmp_le_i32_e32 vcc, v0, v131
	v_or_b32_e32 v0, 0x89, v129
	s_nop 0
	v_cndmask_b32_e32 v54, v206, v102, vcc
	v_cmp_le_i32_e32 vcc, v0, v131
	v_or_b32_e32 v0, 0xa9, v129
	s_nop 0
	v_cndmask_b32_e32 v71, v206, v87, vcc
	v_cmp_le_i32_e32 vcc, v0, v131
	v_or_b32_e32 v0, 0x8a, v129
	s_nop 0
	v_cndmask_b32_e32 v55, v206, v103, vcc
	v_cmp_le_i32_e32 vcc, v0, v131
	v_or_b32_e32 v0, 0xaa, v129
	s_nop 0
	v_cndmask_b32_e32 v72, v206, v88, vcc
	v_cmp_le_i32_e32 vcc, v0, v131
	v_or_b32_e32 v0, 0x8b, v129
	s_nop 0
	v_cndmask_b32_e32 v56, v206, v104, vcc
	v_cmp_le_i32_e32 vcc, v0, v131
	v_or_b32_e32 v0, 0xab, v129
	s_nop 0
	v_cndmask_b32_e32 v73, v206, v89, vcc
	v_cmp_le_i32_e32 vcc, v0, v131
	v_or_b32_e32 v0, 0x90, v129
	v_max3_f32 v82, v82, v72, v73
	s_nop 0
	v_cndmask_b32_e32 v57, v206, v105, vcc
	v_cmp_le_i32_e32 vcc, v0, v131
	v_or_b32_e32 v0, 0xb0, v129
	v_max3_f32 v82, v82, v56, v57
	s_nop 0
	v_cndmask_b32_e32 v74, v206, v90, vcc
	v_cmp_le_i32_e32 vcc, v0, v131
	v_or_b32_e32 v0, 0x91, v129
	s_nop 0
	v_cndmask_b32_e32 v58, v206, v106, vcc
	v_cmp_le_i32_e32 vcc, v0, v131
	v_or_b32_e32 v0, 0xb1, v129
	s_nop 0
	v_cndmask_b32_e32 v75, v206, v91, vcc
	v_cmp_le_i32_e32 vcc, v0, v131
	v_or_b32_e32 v0, 0x92, v129
	s_nop 0
	v_cndmask_b32_e32 v59, v206, v107, vcc
	v_cmp_le_i32_e32 vcc, v0, v131
	v_or_b32_e32 v0, 0xb2, v129
	s_nop 0
	v_cndmask_b32_e32 v76, v206, v92, vcc
	v_cmp_le_i32_e32 vcc, v0, v131
	v_or_b32_e32 v0, 0x93, v129
	s_nop 0
	v_cndmask_b32_e32 v60, v206, v108, vcc
	v_cmp_le_i32_e32 vcc, v0, v131
	v_or_b32_e32 v0, 0xb3, v129
	s_nop 0
	v_cndmask_b32_e32 v77, v206, v93, vcc
	v_cmp_le_i32_e32 vcc, v0, v131
	v_or_b32_e32 v0, 0x98, v129
	v_max3_f32 v82, v82, v76, v77
	s_nop 0
	v_cndmask_b32_e32 v61, v206, v109, vcc
	v_cmp_le_i32_e32 vcc, v0, v131
	v_or_b32_e32 v0, 0xb8, v129
	v_max3_f32 v82, v82, v60, v61
	s_nop 0
	v_cndmask_b32_e32 v78, v206, v94, vcc
	v_cmp_le_i32_e32 vcc, v0, v131
	v_or_b32_e32 v0, 0x99, v129
	s_nop 0
	v_cndmask_b32_e32 v62, v206, v110, vcc
	v_cmp_le_i32_e32 vcc, v0, v131
	v_or_b32_e32 v0, 0xb9, v129
	s_nop 0
	v_cndmask_b32_e32 v79, v206, v95, vcc
	v_cmp_le_i32_e32 vcc, v0, v131
	v_or_b32_e32 v0, 0x9a, v129
	s_nop 0
	v_cndmask_b32_e32 v63, v206, v111, vcc
	v_cmp_le_i32_e32 vcc, v0, v131
	v_or_b32_e32 v0, 0xba, v129
	s_nop 0
	v_cndmask_b32_e32 v80, v206, v96, vcc
	v_cmp_le_i32_e32 vcc, v0, v131
	v_or_b32_e32 v0, 0x9b, v129
	s_nop 0
	v_cndmask_b32_e32 v64, v206, v112, vcc
	v_cmp_le_i32_e32 vcc, v0, v131
	v_or_b32_e32 v0, 0xbb, v129
	s_nop 0
	v_cndmask_b32_e32 v81, v206, v97, vcc
	v_cmp_le_i32_e32 vcc, v0, v131
	v_max3_f32 v0, v66, v67, v50
	v_max3_f32 v82, v82, v80, v81
	s_nop 0
	v_max3_f32 v0, v0, v52, v53
	s_nop 0
	v_max3_f32 v0, v0, v70, v71
	v_cndmask_b32_e32 v65, v206, v113, vcc
	v_max3_f32 v0, v0, v54, v55
	v_max3_f32 v82, v82, v64, v65
	s_nop 0
	v_max3_f32 v0, v0, v74, v75
	v_max_f32_e32 v82, v82, v82
	v_max3_f32 v0, v0, v58, v59
	s_nop 0
	v_max3_f32 v0, v0, v78, v79
	s_nop 0
	v_max3_f32 v0, v0, v62, v63
	s_nop 0
	v_max_f32_e32 v0, v0, v0
	v_max_f32_e32 v0, v0, v82
	v_mov_b32_e32 v82, v0
	s_nop 1
	v_permlane32_swap_b32_e32 v0, v82
	v_max_f32_e32 v82, v82, v82
	v_max_f32_e32 v0, v0, v0
	v_max_f32_e32 v0, v0, v82
	v_cmp_lt_f32_e32 vcc, s54, v0
	s_cbranch_vccnz .LBB0_1229
; __device__ __forceinline__ void pv(f32x16* o, int vb, bf16x8 pa0, bf16x8 pa1, bf16x8 pa2, bf16x8 pa3) {
; #pragma unroll
;     for (int d0 = 0; d0 < 2; ++d0) { s16x4 lo[4], hi[4];
; #pragma unroll
;         for (int ks = 0; ks < 4; ++ks) {
;             asm volatile("ds_read_b64_tr_b16 %0,%1 offset:%c2" : "=&v"(lo[ks]) : "v"(vb), "i"(d0 * 4096 + ks * 1024) : "memory");
;             asm volatile("ds_read_b64_tr_b16 %0,%1 offset:%c2" : "=&v"(hi[ks]) : "v"(vb), "i"(d0 * 4096 + ks * 1024 + 512) : "memory"); }
;         asm volatile("s_waitcnt lgkmcnt(0)" ::: "memory"); __builtin_amdgcn_sched_barrier(0);
;     ...
;         o[d0] = __builtin_amdgcn_mfma_f32_32x32x16_bf16(pa0, MLA_PK(0), o[d0], 0, 0, 0);
;         o[d0] = __builtin_amdgcn_mfma_f32_32x32x16_bf16(pa1, MLA_PK(1), o[d0], 0, 0, 0);
;         o[d0] = __builtin_amdgcn_mfma_f32_32x32x16_bf16(pa2, MLA_PK(2), o[d0], 0, 0, 0);
;         o[d0] = __builtin_amdgcn_mfma_f32_32x32x16_bf16(pa3, MLA_PK(3), o[d0], 0, 0, 0);
;     ...
;     }
; }
.LBB0_1180:
	s_waitcnt vmcnt(1) lgkmcnt(0)
	s_barrier
	s_setprio 1
	ds_read_b128 v[226:229], v130
	ds_read_b128 v[230:233], v130 offset:512
	ds_read_b128 v[234:237], v130 offset:2048
	ds_read_b128 v[238:241], v130 offset:2560
	ds_read_b128 v[242:245], v130 offset:4096
	ds_read_b128 v[246:249], v130 offset:4608
	v_exp_f32_e32 v66, v66
	v_exp_f32_e32 v67, v67
	v_exp_f32_e32 v68, v68
	v_exp_f32_e32 v69, v69
	s_nop 0
	v_exp_f32_e32 v70, v70
	v_exp_f32_e32 v71, v71
	v_exp_f32_e32 v72, v72
	v_exp_f32_e32 v73, v73
	v_exp_f32_e32 v74, v74
	v_exp_f32_e32 v75, v75
	v_exp_f32_e32 v76, v76
	v_exp_f32_e32 v77, v77
	s_waitcnt lgkmcnt(5)
	v_mfma_f32_32x32x16_bf16 v[82:97], v[226:229], v[196:199], v[34:49]
	s_waitcnt lgkmcnt(4)
	v_mfma_f32_32x32x16_bf16 v[34:49], v[230:233], v[196:199], v[34:49]
	ds_read_b128 v[226:229], v130 offset:6144
	ds_read_b128 v[230:233], v130 offset:6656
	v_exp_f32_e32 v78, v78
	v_exp_f32_e32 v79, v79
	v_exp_f32_e32 v80, v80
	v_exp_f32_e32 v81, v81
	s_nop 0
	v_add_f32_e32 v0, 0, v66
	v_add_f32_e32 v0, v67, v0
	v_add_f32_e32 v0, v68, v0
	v_add_f32_e32 v0, v69, v0
	v_add_f32_e32 v0, v0, v70
	v_add_f32_e32 v0, v71, v0
	v_add_f32_e32 v0, v72, v0
	v_exp_f32_e32 v50, v50
	v_exp_f32_e32 v51, v51
	v_exp_f32_e32 v52, v52
	v_exp_f32_e32 v53, v53
	v_add_f32_e32 v0, v73, v0
	s_waitcnt lgkmcnt(5)
	v_mfma_f32_32x32x16_bf16 v[82:97], v[234:237], v[192:195], v[82:97]
	s_waitcnt lgkmcnt(4)
	v_mfma_f32_32x32x16_bf16 v[34:49], v[238:241], v[192:195], v[34:49]
	ds_read_b128 v[234:237], v130 offset:8192
	ds_read_b128 v[238:241], v130 offset:8704
	v_add_f32_e32 v0, v74, v0
	v_add_f32_e32 v0, v75, v0
	v_add_f32_e32 v0, v76, v0
	v_exp_f32_e32 v54, v54
	v_exp_f32_e32 v55, v55
	v_exp_f32_e32 v56, v56
	v_exp_f32_e32 v57, v57
	v_add_f32_e32 v0, v77, v0
	v_cvt_pk_bf16_f32 v160, v66, v67
	v_cvt_pk_bf16_f32 v161, v68, v69
	v_add_f32_e32 v0, v78, v0
	v_add_f32_e32 v0, v79, v0
	v_add_f32_e32 v0, v80, v0
	v_exp_f32_e32 v58, v58
	v_exp_f32_e32 v59, v59
	v_exp_f32_e32 v60, v60
	v_exp_f32_e32 v61, v61
	v_add_f32_e32 v0, v81, v0
	v_cvt_pk_bf16_f32 v162, v70, v71
	v_cvt_pk_bf16_f32 v163, v72, v73
	s_waitcnt lgkmcnt(5)
	v_mfma_f32_32x32x16_bf16 v[82:97], v[242:245], v[188:191], v[82:97]
	s_waitcnt lgkmcnt(4)
	v_mfma_f32_32x32x16_bf16 v[34:49], v[246:249], v[188:191], v[34:49]
	ds_read_b128 v[242:245], v130 offset:10240
	ds_read_b128 v[246:249], v130 offset:10752
	v_exp_f32_e32 v62, v62
	v_exp_f32_e32 v63, v63
	v_exp_f32_e32 v64, v64
	v_exp_f32_e32 v65, v65
	v_cvt_pk_bf16_f32 v164, v74, v75
	v_add_f32_e32 v0, v0, v50
	v_add_f32_e32 v0, v51, v0
	v_add_f32_e32 v0, v52, v0
	v_add_f32_e32 v0, v53, v0
	v_cvt_pk_bf16_f32 v165, v76, v77
	v_add_f32_e32 v0, v0, v54
	v_add_f32_e32 v0, v55, v0
	v_add_f32_e32 v0, v56, v0
	v_add_f32_e32 v0, v57, v0
	v_cvt_pk_bf16_f32 v166, v78, v79
	v_cvt_pk_bf16_f32 v167, v80, v81
	s_waitcnt lgkmcnt(5)
	v_mfma_f32_32x32x16_bf16 v[82:97], v[226:229], v[184:187], v[82:97]
	s_waitcnt lgkmcnt(4)
	v_mfma_f32_32x32x16_bf16 v[34:49], v[230:233], v[184:187], v[34:49]
	v_add_f32_e32 v0, v58, v0
	v_add_f32_e32 v0, v59, v0
	v_add_f32_e32 v0, v60, v0
	v_add_f32_e32 v0, v61, v0
	v_cvt_pk_bf16_f32 v168, v50, v51
	v_cvt_pk_bf16_f32 v169, v52, v53
	v_add_f32_e32 v0, v62, v0
	v_add_f32_e32 v0, v63, v0
	v_add_f32_e32 v0, v64, v0
	v_add_f32_e32 v0, v65, v0
	v_cvt_pk_bf16_f32 v170, v54, v55
	v_cvt_pk_bf16_f32 v171, v56, v57
	s_waitcnt lgkmcnt(3)
	v_mfma_f32_32x32x16_bf16 v[82:97], v[234:237], v[180:183], v[82:97]
	s_waitcnt lgkmcnt(2)
	v_mfma_f32_32x32x16_bf16 v[34:49], v[238:241], v[180:183], v[34:49]
	v_cvt_pk_bf16_f32 v172, v58, v59
	v_cvt_pk_bf16_f32 v173, v60, v61
	s_nop 0
	v_cvt_pk_bf16_f32 v174, v62, v63
	v_cvt_pk_bf16_f32 v175, v64, v65
	s_waitcnt lgkmcnt(1)
	v_mfma_f32_32x32x16_bf16 v[82:97], v[242:245], v[176:179], v[82:97]
	s_waitcnt lgkmcnt(0)
	v_mfma_f32_32x32x16_bf16 v[34:49], v[246:249], v[176:179], v[34:49]
	v_add_f32_e32 v98, v132, v0
	s_setprio 0
	s_addk_i32 s72, 0x4000
	s_and_b32 s0, s72, 0x6000
	v_add_u32_e32 v0, s0, v211
	ds_read_b64_tr_b16 v[50:51],v0 offset:0
	ds_read_b64_tr_b16 v[52:53],v0 offset:512
	ds_read_b64_tr_b16 v[54:55],v0 offset:1024
	ds_read_b64_tr_b16 v[56:57],v0 offset:1536
	ds_read_b64_tr_b16 v[58:59],v0 offset:2048
	ds_read_b64_tr_b16 v[60:61],v0 offset:2560
	ds_read_b64_tr_b16 v[62:63],v0 offset:3072
	ds_read_b64_tr_b16 v[64:65],v0 offset:3584
	s_waitcnt lgkmcnt(0)
	s_nop 0
	v_mfma_f32_32x32x16_bf16 v[2:17], v[160:163], v[50:53], v[2:17]
	ds_read_b64_tr_b16 v[50:51],v0 offset:4096
	ds_read_b64_tr_b16 v[52:53],v0 offset:4608
	v_mfma_f32_32x32x16_bf16 v[2:17], v[164:167], v[54:57], v[2:17]
	ds_read_b64_tr_b16 v[54:55],v0 offset:5120
	ds_read_b64_tr_b16 v[56:57],v0 offset:5632
	v_mfma_f32_32x32x16_bf16 v[2:17], v[168:171], v[58:61], v[2:17]
	ds_read_b64_tr_b16 v[58:59],v0 offset:6144
	ds_read_b64_tr_b16 v[60:61],v0 offset:6656
	ds_read_b64_tr_b16 v[66:67],v0 offset:7168
	ds_read_b64_tr_b16 v[68:69],v0 offset:7680
	s_waitcnt lgkmcnt(0)
; __device__ __forceinline__ float max3f(float a, float b, float c) { float r; asm("v_max3_f32 %0, %1, %2, %3" : "=v"(r) : "v"(a), "v"(b), "v"(c)); return r; }
; __device__ __forceinline__ void cmask(f32x16& p0, f32x16& p1, int jb, int qrel, int hi) {
;     const float NEG = -INFINITY; const int kb = 64 * jb + 4 * hi;
; #pragma unroll
;     for (int r = 0; r < 16; ++r) { const int kv = kb + (r & 3) + 8 * (r >> 2); if (kv > qrel) p0[r] = NEG; if (kv + 32 > qrel) p1[r] = NEG; }
; }
; __device__ __forceinline__ float rowmax(const f32x16& p0, const f32x16& p1) {
;     float a = max3f(p0[0], p0[1], p1[0]), b = max3f(p0[2], p0[3], p1[1]); a = max3f(a, p1[2], p1[3]);
; #pragma unroll
;     for (int r = 4; r < 16; r += 4) { a = max3f(a, p0[r], p0[r + 1]); b = max3f(b, p0[r + 2], p0[r + 3]); a = max3f(a, p1[r], p1[r + 1]); b = max3f(b, p1[r + 2], p1[r + 3]); }
;     const float m = fmaxf(a, b);
;     auto rr = __builtin_amdgcn_permlane32_swap(__float_as_uint(m), __float_as_uint(m), false, false);
;     return fmaxf(__uint_as_float(rr[0]), __uint_as_float(rr[1]));
; }
	v_mfma_f32_32x32x16_bf16 v[2:17], v[172:175], v[62:65], v[2:17]
	v_or_b32_e32 v62, 0xe0, v129
	v_or_b32_e32 v0, 0xc0, v129
	v_cmp_le_i32_e32 vcc, v62, v131
	v_mfma_f32_32x32x16_bf16 v[18:33], v[160:163], v[50:53], v[18:33]
	s_nop 0
	v_cndmask_b32_e32 v34, v206, v34, vcc
	v_cmp_lt_i32_e32 vcc, v0, v131
	s_nop 1
	v_cndmask_b32_e32 v51, v206, v83, vcc
	v_cmp_le_i32_e32 vcc, v0, v131
	v_or_b32_e32 v0, 0xe1, v129
	v_mfma_f32_32x32x16_bf16 v[18:33], v[164:167], v[54:57], v[18:33]
	v_cndmask_b32_e32 v50, v206, v82, vcc
	v_cmp_le_i32_e32 vcc, v0, v131
	v_or_b32_e32 v0, 0xc2, v129
	s_nop 0
	v_cndmask_b32_e32 v35, v206, v35, vcc
	v_cmp_le_i32_e32 vcc, v0, v131
	v_or_b32_e32 v0, 0xe2, v129
	v_mfma_f32_32x32x16_bf16 v[18:33], v[168:171], v[58:61], v[18:33]
	v_cndmask_b32_e32 v52, v206, v84, vcc
	v_cmp_le_i32_e32 vcc, v0, v131
	v_or_b32_e32 v0, 0xc3, v129
	s_nop 0
	v_cndmask_b32_e32 v36, v206, v36, vcc
	v_cmp_le_i32_e32 vcc, v0, v131
	v_or_b32_e32 v0, 0xe3, v129
	v_mfma_f32_32x32x16_bf16 v[18:33], v[172:175], v[66:69], v[18:33]
	v_cndmask_b32_e32 v53, v206, v85, vcc
	v_cmp_le_i32_e32 vcc, v0, v131
	v_or_b32_e32 v0, 0xc8, v129
	v_max3_f32 v66, v52, v53, v35
	s_nop 0
	v_cndmask_b32_e32 v37, v206, v37, vcc
	v_cmp_le_i32_e32 vcc, v0, v131
	v_or_b32_e32 v0, 0xe8, v129
	s_nop 0
	v_cndmask_b32_e32 v54, v206, v86, vcc
	v_cmp_le_i32_e32 vcc, v0, v131
	v_or_b32_e32 v0, 0xc9, v129
	s_nop 0
	v_cndmask_b32_e32 v38, v206, v38, vcc
	v_cmp_le_i32_e32 vcc, v0, v131
	v_or_b32_e32 v0, 0xe9, v129
	s_nop 0
	v_cndmask_b32_e32 v55, v206, v87, vcc
	v_cmp_le_i32_e32 vcc, v0, v131
	v_or_b32_e32 v0, 0xca, v129
	s_nop 0
	v_cndmask_b32_e32 v39, v206, v39, vcc
	v_cmp_le_i32_e32 vcc, v0, v131
	v_or_b32_e32 v0, 0xea, v129
	s_nop 0
	v_cndmask_b32_e32 v56, v206, v88, vcc
	v_cmp_le_i32_e32 vcc, v0, v131
	v_or_b32_e32 v0, 0xcb, v129
	s_nop 0
	v_cndmask_b32_e32 v40, v206, v40, vcc
	v_cmp_le_i32_e32 vcc, v0, v131
	v_or_b32_e32 v0, 0xeb, v129
	s_nop 0
	v_cndmask_b32_e32 v57, v206, v89, vcc
	v_cmp_le_i32_e32 vcc, v0, v131
	v_or_b32_e32 v0, 0xd0, v129
	v_max3_f32 v66, v66, v56, v57
	s_nop 0
	v_cndmask_b32_e32 v41, v206, v41, vcc
	v_cmp_le_i32_e32 vcc, v0, v131
	v_or_b32_e32 v0, 0xf0, v129
	v_max3_f32 v66, v66, v40, v41
	s_nop 0
	v_cndmask_b32_e32 v58, v206, v90, vcc
	v_cmp_le_i32_e32 vcc, v0, v131
	v_or_b32_e32 v0, 0xd1, v129
	s_nop 0
	v_cndmask_b32_e32 v42, v206, v42, vcc
	v_cmp_le_i32_e32 vcc, v0, v131
	v_or_b32_e32 v0, 0xf1, v129
	s_nop 0
	v_cndmask_b32_e32 v59, v206, v91, vcc
	v_cmp_le_i32_e32 vcc, v0, v131
	v_or_b32_e32 v0, 0xd2, v129
	s_nop 0
	v_cndmask_b32_e32 v43, v206, v43, vcc
	v_cmp_le_i32_e32 vcc, v0, v131
	v_or_b32_e32 v0, 0xf2, v129
	s_nop 0
	v_cndmask_b32_e32 v60, v206, v92, vcc
	v_cmp_le_i32_e32 vcc, v0, v131
	v_or_b32_e32 v0, 0xd3, v129
	s_nop 0
	v_cndmask_b32_e32 v44, v206, v44, vcc
	v_cmp_le_i32_e32 vcc, v0, v131
	v_or_b32_e32 v0, 0xf3, v129
	s_nop 0
	v_cndmask_b32_e32 v61, v206, v93, vcc
	v_cmp_le_i32_e32 vcc, v0, v131
	v_or_b32_e32 v0, 0xd8, v129
	v_max3_f32 v66, v66, v60, v61
	s_nop 0
	v_cndmask_b32_e32 v45, v206, v45, vcc
	v_cmp_le_i32_e32 vcc, v0, v131
	v_or_b32_e32 v0, 0xf8, v129
	v_max3_f32 v66, v66, v44, v45
	s_nop 0
	v_cndmask_b32_e32 v62, v206, v94, vcc
	v_cmp_le_i32_e32 vcc, v0, v131
	v_or_b32_e32 v0, 0xd9, v129
	s_nop 0
	v_cndmask_b32_e32 v46, v206, v46, vcc
	v_cmp_le_i32_e32 vcc, v0, v131
	v_or_b32_e32 v0, 0xf9, v129
	s_nop 0
	v_cndmask_b32_e32 v63, v206, v95, vcc
	v_cmp_le_i32_e32 vcc, v0, v131
	v_or_b32_e32 v0, 0xda, v129
	s_nop 0
	v_cndmask_b32_e32 v47, v206, v47, vcc
	v_cmp_le_i32_e32 vcc, v0, v131
	v_or_b32_e32 v0, 0xfa, v129
	s_nop 0
	v_cndmask_b32_e32 v64, v206, v96, vcc
	v_cmp_le_i32_e32 vcc, v0, v131
	v_or_b32_e32 v0, 0xdb, v129
	s_nop 0
	v_cndmask_b32_e32 v48, v206, v48, vcc
	v_cmp_le_i32_e32 vcc, v0, v131
	v_or_b32_e32 v0, 0xfb, v129
	s_nop 0
	v_cndmask_b32_e32 v65, v206, v97, vcc
	v_cmp_le_i32_e32 vcc, v0, v131
	v_max3_f32 v0, v50, v51, v34
	v_max3_f32 v66, v66, v64, v65
	s_nop 0
	v_max3_f32 v0, v0, v36, v37
	s_nop 0
	v_max3_f32 v0, v0, v54, v55
	v_cndmask_b32_e32 v49, v206, v49, vcc
	v_max3_f32 v0, v0, v38, v39
	v_max3_f32 v66, v66, v48, v49
	s_nop 0
	v_max3_f32 v0, v0, v58, v59
	v_max_f32_e32 v66, v66, v66
	v_max3_f32 v0, v0, v42, v43
	s_nop 0
	v_max3_f32 v0, v0, v62, v63
	s_nop 0
	v_max3_f32 v0, v0, v46, v47
	s_nop 0
	v_max_f32_e32 v0, v0, v0
	v_max_f32_e32 v0, v0, v66
	v_mov_b32_e32 v66, v0
	s_nop 1
	v_permlane32_swap_b32_e32 v0, v66
	v_max_f32_e32 v66, v66, v66
	v_max_f32_e32 v0, v0, v0
	v_max_f32_e32 v0, v0, v66
	v_cmp_lt_f32_e32 vcc, s54, v0
	s_cbranch_vccnz .LBB0_1232
